# speedup vs baseline: 1.0171x; 1.0171x over previous
.LBB2_13:
	s_waitcnt vmcnt(0)
	s_barrier
	v_add_u32_e32 v34, s22, v109
	v_add_u32_e32 v34, 0xffff4000, v34
	v_and_b32_e32 v34, 0xc000, v34
	v_add_u32_e32 v114, 0, v34
	v_add_u32_e32 v38, v114, v106
	v_add_u32_e32 v82, v114, v105
	ds_read_b128 v[34:37], v38
	ds_read_b128 v[38:41], v38 offset:4096
	ds_read_b128 v[116:119], v82
	ds_read_b128 v[120:123], v82 offset:4096
	v_add_u32_e32 v82, v114, v104
	s_waitcnt lgkmcnt(2)
	v_mfma_f32_32x32x16_f16 v[50:65], v[34:37], v[78:81], 0
	v_mfma_f32_32x32x16_f16 v[34:49], v[38:41], v[78:81], 0
	s_waitcnt lgkmcnt(1)
	v_mfma_f32_32x32x16_f16 v[50:65], v[116:119], v[74:77], v[50:65]
	s_waitcnt lgkmcnt(0)
	v_mfma_f32_32x32x16_f16 v[34:49], v[120:123], v[74:77], v[34:49]
	ds_read_b128 v[116:119], v82
	ds_read_b128 v[120:123], v82 offset:4096
	v_add_u32_e32 v82, v114, v103
	s_waitcnt lgkmcnt(1)
	v_mfma_f32_32x32x16_f16 v[50:65], v[116:119], v[70:73], v[50:65]
	s_waitcnt lgkmcnt(0)
	v_mfma_f32_32x32x16_f16 v[34:49], v[120:123], v[70:73], v[34:49]
	ds_read_b128 v[116:119], v82
	ds_read_b128 v[120:123], v82 offset:4096
	s_waitcnt lgkmcnt(1)
	v_mfma_f32_32x32x16_f16 v[50:65], v[116:119], v[66:69], v[50:65]
	s_waitcnt lgkmcnt(0)
	v_mfma_f32_32x32x16_f16 v[34:49], v[120:123], v[66:69], v[34:49]
	s_add_i32 s16, s22, 0xffffc000
	s_and_b32 s16, s16, 0xc000
	v_add_u32_e32 v116, s16, v108
	s_add_u32 s16, s12, 0xfffce000
	s_addc_u32 s17, s13, -1
	v_readfirstlane_b32 s26, v116
	v_lshl_add_u64 v[116:117], s[16:17], 0, v[84:85]
	s_mov_b32 s27, m0
	s_mov_b32 m0, s26
	s_nop 0
	global_load_lds_dwordx4 v[116:117], off
	s_mov_b32 m0, s27
	v_lshl_add_u64 v[116:117], s[16:17], 0, v[86:87]
	s_add_i32 s16, s26, 0x400
	s_mov_b32 s17, m0
	s_mov_b32 m0, s16
	s_nop 0
	global_load_lds_dwordx4 v[116:117], off
	s_mov_b32 m0, s17
	s_and_b32 s16, s22, 0xc000
	v_add_u32_e32 v116, s16, v108
	s_nop 0
	v_readfirstlane_b32 s16, v116
	v_lshl_add_u64 v[116:117], s[12:13], 0, v[84:85]
	s_mov_b32 s17, m0
	s_mov_b32 m0, s16
	s_nop 0
	global_load_lds_dwordx4 v[116:117], off
	s_mov_b32 m0, s17
	v_lshl_add_u64 v[116:117], s[12:13], 0, v[86:87]
	s_addk_i32 s16, 0x400
	s_mov_b32 s17, m0
	s_mov_b32 m0, s16
	s_nop 0
	global_load_lds_dwordx4 v[116:117], off
	s_mov_b32 m0, s17
	v_max3_f32 v82, v50, v51, v52
	v_max3_f32 v82, v82, v53, v54
	v_max3_f32 v82, v82, v55, v56
	v_max3_f32 v82, v82, v57, v58
	v_max3_f32 v82, v82, v59, v60
	v_max3_f32 v82, v82, v61, v62
	v_max_f32_e32 v91, v65, v65
	v_max3_f32 v89, v34, v35, v36
	v_max3_f32 v89, v89, v37, v38
	v_max3_f32 v89, v89, v39, v40
	v_max3_f32 v89, v89, v41, v42
	v_max3_f32 v89, v89, v43, v44
	v_max3_f32 v89, v89, v45, v46
	v_max_f32_e32 v90, v49, v49
	v_max3_f32 v82, v82, v63, v64
	v_max3_f32 v89, v89, v47, v48
	v_max_f32_e32 v90, v91, v90
	v_max3_f32 v82, v82, v89, v90
	v_mov_b32_e32 v89, v82
	s_nop 1
	v_permlane32_swap_b32_e32 v82, v89
	v_max_f32_e32 v82, v82, v89
	v_fma_f32 v89, v82, s23, -v88
	v_cmp_lt_f32_e32 vcc, s24, v89
	s_cbranch_vccz .LBB2_16
	v_mul_f32_e32 v82, 0x3e38aa3b, v82
	v_max_f32_e32 v82, v82, v82
	v_max_f32_e32 v89, v88, v88
	v_max_f32_e32 v102, v89, v82
	v_sub_f32_e32 v82, v88, v102
	v_exp_f32_e32 v82, v82
	s_and_saveexec_b64 s[16:17], s[4:5]
	s_cbranch_execz .LBB2_11
	v_lshl_add_u32 v88, v95, 2, v100
	ds_write_b32 v88, v82
	s_branch .LBB2_11

.LBB7_3:
	s_ashr_i32 s44, s23, 31
	s_xor_b32 s44, s44, s25
	s_abs_i32 s45, s23
	s_mul_hi_u32 s48, s45, s26
	s_mul_i32 s49, s48, s24
	s_sub_i32 s45, s45, s49
	s_add_i32 s49, s48, 1
	s_sub_i32 s46, s45, s24
	s_cmp_ge_u32 s45, s24
	s_cselect_b32 s48, s49, s48
	s_cselect_b32 s45, s46, s45
	s_add_i32 s49, s48, 1
	s_cmp_ge_u32 s45, s24
	s_cselect_b32 s45, s49, s48
	s_xor_b32 s45, s45, s44
	s_sub_i32 s44, s45, s44
	s_mul_i32 s45, s44, s21
	s_sub_i32 s47, s23, s45
	s_lshl_b32 s48, s47, 7
	s_lshl_b32 s46, s44, 7
	s_ashr_i32 s49, s48, 31
	v_or_b32_e32 v152, s46, v1
	v_lshl_add_u64 v[154:155], s[48:49], 1, v[70:71]
	v_mad_i64_i32 v[156:157], s[50:51], v152, s29, v[154:155]
	v_lshl_add_u64 v[158:159], s[48:49], 2, v[68:69]
	v_or_b32_e32 v153, 32, v152
	global_load_dwordx4 v[160:163], v[156:157], off
	v_mad_i64_i32 v[184:185], s[50:51], v153, s29, v[154:155]
	v_or_b32_e32 v153, 64, v152
	global_load_dwordx4 v[176:179], v[158:159], off
	global_load_dwordx4 v[180:183], v[158:159], off offset:16
	v_mad_i64_i32 v[186:187], s[50:51], v153, s29, v[154:155]
	v_or_b32_e32 v153, 0x60, v152
	global_load_dwordx4 v[164:167], v[184:185], off
	v_mad_i64_i32 v[188:189], s[50:51], v153, s29, v[154:155]
	global_load_dwordx4 v[168:171], v[186:187], off
	s_nop 0
	global_load_dwordx4 v[172:175], v[188:189], off
	v_add_u32_e32 v67, v80, v77
	s_waitcnt vmcnt(14)
	s_barrier
	s_waitcnt lgkmcnt(0)
	ds_read_b128 v[2:5], v67 offset:16384
	v_add_u32_e32 v109, v79, v77
	ds_read_b128 v[6:9], v109
	ds_read_b128 v[10:13], v109 offset:4096
	ds_read_b128 v[14:17], v67 offset:20480
	v_add_u32_e32 v126, v80, v76
	ds_read_b128 v[34:37], v126 offset:16384
	v_add_u32_e32 v127, v79, v76
	s_waitcnt lgkmcnt(3)
	v_mfma_f32_32x32x16_f16 v[50:65], v[2:5], v[6:9], 0
	ds_read_b128 v[110:113], v127
	ds_read_b128 v[114:117], v127 offset:4096
	ds_read_b128 v[118:121], v126 offset:20480
	v_readfirstlane_b32 s2, v0
	s_lshl_b32 s19, s27, 15
	s_lshl_b32 s2, s2, 4
	s_add_i32 s1, s19, 0
	s_and_b32 s31, s2, 0xfffffc00
	s_add_i32 s1, s1, s31
	s_waitcnt lgkmcnt(5)
	v_mfma_f32_32x32x16_f16 v[18:33], v[2:5], v[10:13], 0
	s_mov_b32 m0, s1
	s_add_i32 s2, s1, 0x2000
	buffer_load_dwordx4 v72, s[4:7], s0 offen lds
	s_mov_b32 m0, s2
	s_add_i32 s3, s1, 0x4000
	buffer_load_dwordx4 v74, s[4:7], s0 offen lds
	s_mov_b32 s14, s10
	s_waitcnt lgkmcnt(2)
	v_mfma_f32_32x32x16_f16 v[50:65], v[34:37], v[110:113], v[50:65]
	s_mov_b32 s15, s11
	s_mov_b32 m0, s3
	s_add_i32 s18, s1, 0x6000
	buffer_load_dwordx4 v73, s[12:15], s0 offen lds
	s_mov_b32 m0, s18
	s_add_i32 s33, s19, 0x8000
	buffer_load_dwordx4 v75, s[12:15], s0 offen lds
	s_waitcnt lgkmcnt(1)
	v_mfma_f32_32x32x16_f16 v[18:33], v[34:37], v[114:117], v[18:33]
	s_waitcnt vmcnt(14)
	s_barrier
	s_and_b32 s33, s33, 0x18000
	s_add_i32 s33, s33, 0
	s_add_i32 s33, s33, s31
	s_add_i32 s34, s0, 0x80
	s_mov_b32 m0, s33
	v_mfma_f32_32x32x16_f16 v[34:49], v[14:17], v[6:9], 0
	v_add_u32_e32 v128, v81, v77
	v_add_u32_e32 v129, v82, v77
	v_add_u32_e32 v130, v81, v76
	v_add_u32_e32 v131, v82, v76
	s_xor_b32 s19, s19, 0x10000
	v_add_u32_e32 v134, v83, v77
	v_add_u32_e32 v138, v84, v77
	v_mfma_f32_32x32x16_f16 v[2:17], v[14:17], v[10:13], 0
	v_add_u32_e32 v142, v83, v76
	v_add_u32_e32 v146, v84, v76
	s_waitcnt lgkmcnt(0)
	v_mfma_f32_32x32x16_f16 v[34:49], v[118:121], v[110:113], v[34:49]
	v_mfma_f32_32x32x16_f16 v[2:17], v[118:121], v[114:117], v[2:17]
	ds_read_b128 v[110:113], v67 offset:49152
	ds_read_b128 v[114:117], v109 offset:32768
	ds_read_b128 v[118:121], v109 offset:36864
	ds_read_b128 v[122:125], v67 offset:53248
	s_waitcnt lgkmcnt(2)
	v_mfma_f32_32x32x16_f16 v[50:65], v[110:113], v[114:117], v[50:65]
	s_waitcnt lgkmcnt(1)
	v_mfma_f32_32x32x16_f16 v[18:33], v[110:113], v[118:121], v[18:33]
	s_waitcnt lgkmcnt(0)
	v_mfma_f32_32x32x16_f16 v[34:49], v[122:125], v[114:117], v[34:49]
	v_mfma_f32_32x32x16_f16 v[2:17], v[122:125], v[118:121], v[2:17]
	ds_read_b128 v[110:113], v126 offset:49152
	ds_read_b128 v[114:117], v127 offset:32768
	ds_read_b128 v[118:121], v127 offset:36864
	ds_read_b128 v[122:125], v126 offset:53248
	buffer_load_dwordx4 v72, s[4:7], s34 offen lds
	s_add_i32 m0, s33, 0x2000
	s_nop 0
	buffer_load_dwordx4 v74, s[4:7], s34 offen lds
	s_add_i32 m0, s33, 0x4000
	s_nop 0
	buffer_load_dwordx4 v73, s[12:15], s34 offen lds
	s_add_i32 m0, s33, 0x6000
	s_waitcnt lgkmcnt(2)
	v_mfma_f32_32x32x16_f16 v[50:65], v[110:113], v[114:117], v[50:65]
	buffer_load_dwordx4 v75, s[12:15], s34 offen lds
	s_waitcnt vmcnt(14)
	s_barrier
	s_add_i32 s33, s19, 0
	s_add_i32 s33, s33, s31
	s_add_i32 s34, s0, 0x100
	s_mov_b32 m0, s33
	s_waitcnt lgkmcnt(1)
	v_mfma_f32_32x32x16_f16 v[18:33], v[110:113], v[118:121], v[18:33]
	ds_read_b128 v[110:113], v96
	s_add_i32 s19, s19, 0x8000
	s_and_b32 s19, s19, 0x18000
	s_add_i32 s19, s19, 0
	s_add_i32 s19, s19, s31
	s_add_i32 s31, s0, 0x180
	s_waitcnt lgkmcnt(1)
	v_mfma_f32_32x32x16_f16 v[34:49], v[122:125], v[114:117], v[34:49]
	v_mfma_f32_32x32x16_f16 v[2:17], v[122:125], v[118:121], v[2:17]
	ds_read_b128 v[114:117], v128
	ds_read_b128 v[118:121], v128 offset:4096
	ds_read_b128 v[122:125], v129 offset:4096
	s_waitcnt lgkmcnt(2)
	v_mfma_f32_32x32x16_f16 v[50:65], v[110:113], v[114:117], v[50:65]
	s_waitcnt lgkmcnt(1)
	v_mfma_f32_32x32x16_f16 v[18:33], v[110:113], v[118:121], v[18:33]
	ds_read_b128 v[110:113], v97
	s_waitcnt lgkmcnt(1)
	v_mfma_f32_32x32x16_f16 v[34:49], v[122:125], v[114:117], v[34:49]
	v_mfma_f32_32x32x16_f16 v[2:17], v[122:125], v[118:121], v[2:17]
	ds_read_b128 v[114:117], v130
	ds_read_b128 v[118:121], v130 offset:4096
	ds_read_b128 v[122:125], v131 offset:4096
	buffer_load_dwordx4 v72, s[4:7], s34 offen lds
	s_add_i32 m0, s33, 0x2000
	s_nop 0
	buffer_load_dwordx4 v74, s[4:7], s34 offen lds
	s_add_i32 m0, s33, 0x4000
	s_waitcnt lgkmcnt(2)
	v_mfma_f32_32x32x16_f16 v[50:65], v[110:113], v[114:117], v[50:65]
	buffer_load_dwordx4 v73, s[12:15], s34 offen lds
	s_add_i32 m0, s33, 0x6000
	s_nop 0
	buffer_load_dwordx4 v75, s[12:15], s34 offen lds
	s_waitcnt vmcnt(8)
	s_barrier
	s_mov_b32 m0, s19
	s_waitcnt lgkmcnt(1)
	v_mfma_f32_32x32x16_f16 v[18:33], v[110:113], v[118:121], v[18:33]
	ds_read_b128 v[110:113], v98
	s_waitcnt lgkmcnt(1)
	v_mfma_f32_32x32x16_f16 v[34:49], v[122:125], v[114:117], v[34:49]
	v_mfma_f32_32x32x16_f16 v[2:17], v[122:125], v[118:121], v[2:17]
	ds_read_b128 v[114:117], v134
	ds_read_b128 v[118:121], v134 offset:4096
	ds_read_b128 v[122:125], v138 offset:4096
	s_waitcnt lgkmcnt(2)
	v_mfma_f32_32x32x16_f16 v[50:65], v[110:113], v[114:117], v[50:65]
	s_waitcnt lgkmcnt(1)
	v_mfma_f32_32x32x16_f16 v[18:33], v[110:113], v[118:121], v[18:33]
	ds_read_b128 v[110:113], v99
	s_waitcnt lgkmcnt(1)
	v_mfma_f32_32x32x16_f16 v[34:49], v[122:125], v[114:117], v[34:49]
	v_mfma_f32_32x32x16_f16 v[2:17], v[122:125], v[118:121], v[2:17]
	ds_read_b128 v[114:117], v142
	ds_read_b128 v[118:121], v142 offset:4096
	ds_read_b128 v[122:125], v146 offset:4096
	buffer_load_dwordx4 v72, s[4:7], s31 offen lds
	s_add_i32 m0, s19, 0x2000
	s_nop 0
	buffer_load_dwordx4 v74, s[4:7], s31 offen lds
	s_add_i32 m0, s19, 0x4000
	s_waitcnt lgkmcnt(2)
	v_mfma_f32_32x32x16_f16 v[50:65], v[110:113], v[114:117], v[50:65]
	buffer_load_dwordx4 v73, s[12:15], s31 offen lds
	s_add_i32 m0, s19, 0x6000
	s_nop 0
	buffer_load_dwordx4 v75, s[12:15], s31 offen lds
	s_waitcnt vmcnt(8)
	s_barrier
	s_add_i32 s31, s0, 0x200
	s_waitcnt lgkmcnt(1)
	v_mfma_f32_32x32x16_f16 v[18:33], v[110:113], v[118:121], v[18:33]
	s_mov_b32 m0, s1
	s_abs_i32 s1, s23
	s_ashr_i32 s0, s23, 31
	s_xor_b32 s0, s0, s25
	s_waitcnt lgkmcnt(0)
	v_mfma_f32_32x32x16_f16 v[2:17], v[122:125], v[118:121], v[2:17]
	v_mfma_f32_32x32x16_f16 v[34:49], v[122:125], v[114:117], v[34:49]
	ds_read_b128 v[110:113], v67 offset:16384
	ds_read_b128 v[114:117], v109
	ds_read_b128 v[118:121], v109 offset:4096
	ds_read_b128 v[122:125], v67 offset:20480
	s_waitcnt lgkmcnt(2)
	v_mfma_f32_32x32x16_f16 v[50:65], v[110:113], v[114:117], v[50:65]
	s_waitcnt lgkmcnt(1)
	v_mfma_f32_32x32x16_f16 v[18:33], v[110:113], v[118:121], v[18:33]
	s_waitcnt lgkmcnt(0)
	v_mfma_f32_32x32x16_f16 v[2:17], v[122:125], v[118:121], v[2:17]
	v_mfma_f32_32x32x16_f16 v[34:49], v[122:125], v[114:117], v[34:49]
	ds_read_b128 v[110:113], v126 offset:16384
	ds_read_b128 v[114:117], v127
	ds_read_b128 v[118:121], v127 offset:4096
	ds_read_b128 v[122:125], v126 offset:20480
	buffer_load_dwordx4 v72, s[4:7], s31 offen lds
	s_mov_b32 m0, s2
	s_mul_hi_u32 s2, s1, s26
	buffer_load_dwordx4 v74, s[4:7], s31 offen lds
	s_mov_b32 m0, s3
	s_mul_i32 s3, s2, s24
	s_waitcnt lgkmcnt(2)
	v_mfma_f32_32x32x16_f16 v[50:65], v[110:113], v[114:117], v[50:65]
	buffer_load_dwordx4 v73, s[12:15], s31 offen lds
	s_mov_b32 m0, s18
	s_sub_i32 s1, s1, s3
	buffer_load_dwordx4 v75, s[12:15], s31 offen lds
	s_waitcnt vmcnt(8)
	s_barrier
	s_add_i32 s3, s2, 1
	s_waitcnt lgkmcnt(1)
	v_mfma_f32_32x32x16_f16 v[18:33], v[110:113], v[118:121], v[18:33]
	s_sub_i32 s14, s1, s24
	s_cmp_ge_u32 s1, s24
	s_cselect_b32 s2, s3, s2
	s_cselect_b32 s1, s14, s1
	s_add_i32 s3, s2, 1
	s_cmp_ge_u32 s1, s24
	s_cselect_b32 s1, s3, s2
	s_waitcnt lgkmcnt(0)
	v_mfma_f32_32x32x16_f16 v[2:17], v[122:125], v[118:121], v[2:17]
	s_xor_b32 s1, s1, s0
	s_sub_i32 s0, s1, s0
	s_mul_i32 s1, s0, s21
	s_sub_i32 s15, s23, s1
	s_lshl_b32 s2, s15, 7
	s_lshl_b32 s14, s0, 7
	s_ashr_i32 s3, s2, 31
	v_mfma_f32_32x32x16_f16 v[34:49], v[122:125], v[114:117], v[34:49]
	ds_read_b128 v[110:113], v67 offset:49152
	ds_read_b128 v[114:117], v109 offset:32768
	ds_read_b128 v[118:121], v109 offset:36864
	ds_read_b128 v[122:125], v67 offset:53248
	s_waitcnt lgkmcnt(2)
	v_mfma_f32_32x32x16_f16 v[50:65], v[110:113], v[114:117], v[50:65]
	s_waitcnt lgkmcnt(1)
	v_mfma_f32_32x32x16_f16 v[18:33], v[110:113], v[118:121], v[18:33]
	s_waitcnt lgkmcnt(0)
	v_mfma_f32_32x32x16_f16 v[2:17], v[122:125], v[118:121], v[2:17]
	v_mfma_f32_32x32x16_f16 v[34:49], v[122:125], v[114:117], v[34:49]
	ds_read_b128 v[110:113], v126 offset:49152
	ds_read_b128 v[114:117], v127 offset:32768
	ds_read_b128 v[118:121], v127 offset:36864
	ds_read_b128 v[122:125], v126 offset:53248
	s_waitcnt vmcnt(4)
	s_barrier
	s_waitcnt lgkmcnt(2)
	v_mfma_f32_32x32x16_f16 v[50:65], v[110:113], v[114:117], v[50:65]
	s_waitcnt lgkmcnt(1)
	v_mfma_f32_32x32x16_f16 v[18:33], v[110:113], v[118:121], v[18:33]
	s_waitcnt lgkmcnt(0)
	v_mfma_f32_32x32x16_f16 v[2:17], v[122:125], v[118:121], v[2:17]
	v_mfma_f32_32x32x16_f16 v[34:49], v[122:125], v[114:117], v[34:49]
	ds_read_b128 v[110:113], v96
	ds_read_b128 v[114:117], v128
	ds_read_b128 v[118:121], v128 offset:4096
	ds_read_b128 v[122:125], v129 offset:4096
	s_waitcnt lgkmcnt(2)
	v_mfma_f32_32x32x16_f16 v[50:65], v[110:113], v[114:117], v[50:65]
	s_waitcnt lgkmcnt(1)
	v_mfma_f32_32x32x16_f16 v[18:33], v[110:113], v[118:121], v[18:33]
	s_waitcnt lgkmcnt(0)
	v_mfma_f32_32x32x16_f16 v[2:17], v[122:125], v[118:121], v[2:17]
	v_mfma_f32_32x32x16_f16 v[34:49], v[122:125], v[114:117], v[34:49]
	ds_read_b128 v[110:113], v97
	ds_read_b128 v[114:117], v130
	ds_read_b128 v[126:129], v130 offset:4096
	ds_read_b128 v[130:133], v131 offset:4096
	s_waitcnt vmcnt(0)
	s_barrier
	s_waitcnt lgkmcnt(2)
	v_mfma_f32_32x32x16_f16 v[50:65], v[110:113], v[114:117], v[50:65]
	s_waitcnt lgkmcnt(1)
	v_mfma_f32_32x32x16_f16 v[18:33], v[110:113], v[126:129], v[18:33]
	s_waitcnt lgkmcnt(0)
	v_mfma_f32_32x32x16_f16 v[2:17], v[130:133], v[126:129], v[2:17]
	v_mfma_f32_32x32x16_f16 v[34:49], v[130:133], v[114:117], v[34:49]
	ds_read_b128 v[110:113], v98
	ds_read_b128 v[114:117], v134
	ds_read_b128 v[134:137], v134 offset:4096
	ds_read_b128 v[138:141], v138 offset:4096
	s_waitcnt lgkmcnt(2)
	v_mfma_f32_32x32x16_f16 v[50:65], v[110:113], v[114:117], v[50:65]
	s_waitcnt lgkmcnt(1)
	v_mfma_f32_32x32x16_f16 v[18:33], v[110:113], v[134:137], v[18:33]
	s_waitcnt lgkmcnt(0)
	v_mfma_f32_32x32x16_f16 v[2:17], v[138:141], v[134:137], v[2:17]
	v_mfma_f32_32x32x16_f16 v[34:49], v[138:141], v[114:117], v[34:49]
	ds_read_b128 v[110:113], v99
	ds_read_b128 v[114:117], v142
	ds_read_b128 v[142:145], v142 offset:4096
	ds_read_b128 v[146:149], v146 offset:4096
	s_waitcnt lgkmcnt(0)
	s_barrier
	s_waitcnt lgkmcnt(2)
	v_mfma_f32_32x32x16_f16 v[50:65], v[110:113], v[114:117], v[50:65]
	s_nop 11
	ds_write_b128 v100, v[50:53]
	ds_write_b128 v101, v[54:57]
	s_waitcnt lgkmcnt(3)
	v_mfma_f32_32x32x16_f16 v[18:33], v[110:113], v[142:145], v[18:33]
	s_waitcnt lgkmcnt(2)
	v_mfma_f32_32x32x16_f16 v[2:17], v[146:149], v[142:145], v[2:17]
	v_mfma_f32_32x32x16_f16 v[34:49], v[146:149], v[114:117], v[34:49]
	ds_write_b128 v102, v[58:61]
	ds_write_b128 v103, v[62:65]
	s_nop 9
	ds_write_b128 v104, v[34:37]
	ds_write_b128 v105, v[38:41]
	ds_write_b128 v106, v[42:45]
	ds_write_b128 v107, v[46:49]
	ds_write_b128 v100, v[18:21] offset:16384
	ds_write_b128 v101, v[22:25] offset:16384
	ds_write_b128 v102, v[26:29] offset:16384
	ds_write_b128 v103, v[30:33] offset:16384
	ds_write_b128 v104, v[2:5] offset:16384
	ds_write_b128 v105, v[6:9] offset:16384
	ds_write_b128 v106, v[10:13] offset:16384
	ds_write_b128 v107, v[14:17] offset:16384
	v_or_b32_e32 v25, s14, v1
	v_lshl_add_u64 v[22:23], s[2:3], 1, v[70:71]
	s_waitcnt lgkmcnt(0)
	s_barrier
	v_mad_i64_i32 v[2:3], s[0:1], v25, s29, v[22:23]
	v_mov_b64_e32 v[10:11], v[160:161]
	v_mov_b64_e32 v[12:13], v[162:163]
	v_lshl_add_u64 v[14:15], s[2:3], 2, v[68:69]
	v_mov_b64_e32 v[6:7], v[176:177]
	v_mov_b64_e32 v[8:9], v[178:179]
	v_mov_b64_e32 v[2:3], v[180:181]
	v_mov_b64_e32 v[4:5], v[182:183]
	v_add_u32_e32 v14, 0, v85
	v_add_u32_e32 v18, s28, v85
	ds_read_b128 v[14:17], v14
	ds_read_b128 v[26:29], v18
	v_or_b32_e32 v18, 32, v25
	v_mad_i64_i32 v[18:19], s[0:1], v18, s29, v[22:23]
	v_mov_b64_e32 v[18:19], v[164:165]
	v_mov_b64_e32 v[20:21], v[166:167]
	s_waitcnt lgkmcnt(0)
	v_pk_add_f32 v[16:17], v[16:17], v[28:29]
	v_add_f32_e32 v35, v14, v26
	v_mov_b32_e32 v34, v27
	v_xor_b32_e32 v24, 8, v108
	v_cvt_f32_f16_e32 v30, v11
	v_cvt_f32_f16_sdwa v31, v11 dst_sel:DWORD dst_unused:UNUSED_PAD src0_sel:WORD_1
	v_add_u32_e32 v11, 0, v86
	v_pk_add_f32 v[16:17], v[8:9], v[16:17]
	ds_read_b128 v[26:29], v11
	v_add_u32_e32 v11, s28, v86
	v_pk_add_f32 v[36:37], v[16:17], v[30:31]
	ds_read_b128 v[30:33], v11
	v_cvt_f32_f16_e32 v38, v13
	v_cvt_f32_f16_sdwa v39, v13 dst_sel:DWORD dst_unused:UNUSED_PAD src0_sel:WORD_1
	v_mov_b32_e32 v16, v2
	v_mov_b32_e32 v17, v3
	s_waitcnt lgkmcnt(0)
	v_pk_add_f32 v[28:29], v[28:29], v[32:33]
	v_cvt_f32_f16_e32 v32, v10
	v_pk_add_f32 v[28:29], v[4:5], v[28:29]
	v_pk_mov_b32 v[16:17], v[26:27], v[16:17] op_sel:[1,0]
	v_pk_add_f32 v[28:29], v[28:29], v[38:39]
	v_cvt_f32_f16_e32 v38, v12
	v_add_f32_e32 v26, v26, v30
	v_cvt_f32_f16_sdwa v33, v10 dst_sel:DWORD dst_unused:UNUSED_PAD src0_sel:WORD_1
	v_cvt_f32_f16_sdwa v30, v12 dst_sel:DWORD dst_unused:UNUSED_PAD src0_sel:WORD_1
	v_or_b32_e32 v12, 64, v25
	v_pk_mov_b32 v[14:15], v[14:15], v[6:7] op_sel:[1,0]
	v_mad_i64_i32 v[40:41], s[0:1], v12, s29, v[22:23]
	v_or_b32_e32 v12, 0x60, v25
	v_mov_b32_e32 v10, v31
	v_mov_b32_e32 v11, v26
	v_mad_i64_i32 v[42:43], s[0:1], v12, s29, v[22:23]
	v_pk_add_f32 v[44:45], v[14:15], v[34:35]
	v_mov_b32_e32 v12, v7
	v_mov_b32_e32 v13, v32
	v_pk_add_f32 v[10:11], v[16:17], v[10:11]
	v_pk_add_f32 v[46:47], v[12:13], v[44:45]
	v_mov_b32_e32 v22, v3
	v_mov_b32_e32 v23, v38
	v_pk_add_f32 v[48:49], v[22:23], v[10:11]
	v_mov_b32_e32 v10, v33
	v_mov_b32_e32 v11, v47
	v_pk_add_f32 v[50:51], v[46:47], v[10:11]
	v_mov_b64_e32 v[14:15], v[168:169]
	v_mov_b64_e32 v[16:17], v[170:171]
	v_mov_b64_e32 v[10:11], v[172:173]
	v_mov_b64_e32 v[12:13], v[174:175]
	v_mov_b32_e32 v31, v49
	v_pk_add_f32 v[40:41], v[48:49], v[30:31]
	v_pk_mov_b32 v[30:31], v[34:35], v[44:45] op_sel:[1,0]
	v_mov_b32_e32 v27, v44
	v_mov_b32_e32 v3, v7
	v_pk_add_f32 v[30:31], v[6:7], v[30:31]
	v_mov_b32_e32 v39, v33
	v_pk_add_f32 v[26:27], v[2:3], v[26:27]
	v_pk_add_f32 v[30:31], v[30:31], v[32:33]
	v_pk_add_f32 v[26:27], v[26:27], v[38:39]
	v_pk_mul_f32 v[32:33], v[46:47], v[46:47]
	v_pk_add_f32 v[34:35], v[30:31], v[26:27]
	v_pk_mul_f32 v[26:27], v[30:31], v[26:27]
	v_mov_b32_e32 v51, v33
	v_pk_mul_f32 v[32:33], v[48:49], v[48:49]
	v_mov_b32_e32 v35, v27
	v_pk_mul_f32 v[26:27], v[40:41], v[40:41]
	v_mov_b32_e32 v32, v40
	v_mov_b32_e32 v67, v26
	v_pk_add_f32 v[32:33], v[50:51], v[32:33]
	v_pk_add_f32 v[26:27], v[34:35], v[66:67]
	v_pk_mul_f32 v[30:31], v[36:37], v[36:37]
	v_pk_mul_f32 v[34:35], v[28:29], v[28:29]
	v_and_b32_e32 v23, 64, v108
	v_pk_add_f32 v[26:27], v[32:33], v[26:27]
	v_mov_b32_e32 v32, v36
	v_mov_b32_e32 v33, v30
	v_mov_b32_e32 v38, v28
	v_mov_b32_e32 v39, v34
	v_add_u32_e32 v23, 64, v23
	v_pk_add_f32 v[32:33], v[32:33], v[38:39]
	v_mov_b32_e32 v30, v37
	v_mov_b32_e32 v34, v29
	v_cmp_lt_i32_e64 s[0:1], v24, v23
	v_pk_add_f32 v[26:27], v[26:27], v[32:33]
	v_pk_add_f32 v[30:31], v[30:31], v[34:35]
	v_cndmask_b32_e64 v24, v108, v24, s[0:1]
	v_pk_add_f32 v[26:27], v[26:27], v[30:31]
	v_lshlrev_b32_e32 v30, 2, v24
	ds_bpermute_b32 v32, v30, v26
	ds_bpermute_b32 v33, v30, v27
	v_xor_b32_e32 v24, 4, v108
	v_cmp_lt_i32_e64 s[0:1], v24, v23
	v_cvt_pk_f16_f32 v39, v28, v29
	v_or_b32_e32 v31, s2, v78
	v_cndmask_b32_e64 v24, v108, v24, s[0:1]
	s_waitcnt lgkmcnt(0)
	v_pk_add_f32 v[26:27], v[26:27], v[32:33]
	v_lshlrev_b32_e32 v32, 2, v24
	ds_bpermute_b32 v34, v32, v26
	ds_bpermute_b32 v35, v32, v27
	v_xor_b32_e32 v24, 2, v108
	v_cmp_lt_i32_e64 s[0:1], v24, v23
	v_cvt_pk_f16_f32 v37, v36, v37
	v_cvt_pk_f16_f32 v36, v47, v50
	v_cndmask_b32_e64 v24, v108, v24, s[0:1]
	s_waitcnt lgkmcnt(0)
	v_pk_add_f32 v[26:27], v[26:27], v[34:35]
	v_lshlrev_b32_e32 v33, 2, v24
	ds_bpermute_b32 v28, v33, v26
	ds_bpermute_b32 v29, v33, v27
	v_mul_lo_u32 v24, v25, s30
	v_add_lshl_u32 v24, v31, v24, 1
	v_cvt_pk_f16_f32 v38, v49, v40
	buffer_store_dwordx4 v[36:39], v24, s[8:11], 0 offen sc1
	s_waitcnt lgkmcnt(0)
	v_pk_add_f32 v[26:27], v[26:27], v[28:29]
	v_xor_b32_e32 v28, 1, v108
	v_cmp_lt_i32_e64 s[0:1], v28, v23
	s_lshl_b32 s2, s15, 4
	v_mov_b32_e32 v24, v7
	v_cndmask_b32_e64 v23, v108, v28, s[0:1]
	v_lshlrev_b32_e32 v34, 2, v23
	ds_bpermute_b32 v28, v34, v26
	ds_bpermute_b32 v29, v34, v27
	s_and_saveexec_b64 s[0:1], vcc
	s_cbranch_execz .LBB7_5
	s_waitcnt lgkmcnt(0)
	v_pk_add_f32 v[64:65], v[26:27], v[28:29]
	v_lshl_add_u32 v23, v25, 6, s2
	v_mov_b32_e32 v67, v66
	s_mov_b32 s18, s10
	s_mov_b32 s19, s11
	buffer_store_dwordx4 v[64:67], v23, s[16:19], 0 offen sc1
.LBB7_5:
	s_or_b64 exec, exec, s[0:1]
	v_add_u32_e32 v23, 0, v88
	v_add_u32_e32 v25, s28, v88
	s_waitcnt lgkmcnt(0)
	ds_read_b128 v[26:29], v23
	ds_read_b128 v[36:39], v25
	v_add_u32_e32 v23, 0, v89
	v_add_u32_e32 v25, s28, v89
	ds_read_b128 v[40:43], v23
	ds_read_b128 v[44:47], v25
	v_cvt_f32_f16_e32 v50, v18
	s_waitcnt lgkmcnt(2)
	v_add_f32_e32 v49, v26, v36
	v_cvt_f32_f16_sdwa v51, v18 dst_sel:DWORD dst_unused:UNUSED_PAD src0_sel:WORD_1
	v_cvt_f32_f16_sdwa v55, v19 dst_sel:DWORD dst_unused:UNUSED_PAD src0_sel:WORD_1
	v_cvt_f32_f16_e32 v54, v19
	v_pk_mov_b32 v[26:27], v[26:27], v[6:7] op_sel:[1,0]
	v_mov_b32_e32 v48, v37
	v_cvt_f32_f16_e32 v52, v20
	v_pk_add_f32 v[26:27], v[26:27], v[48:49]
	v_pk_add_f32 v[28:29], v[28:29], v[38:39]
	v_pk_mov_b32 v[36:37], v[48:49], v[26:27] op_sel:[1,0]
	s_waitcnt lgkmcnt(0)
	v_add_f32_e32 v18, v40, v44
	v_pk_add_f32 v[28:29], v[8:9], v[28:29]
	v_pk_add_f32 v[36:37], v[6:7], v[36:37]
	v_mov_b32_e32 v25, v50
	v_cvt_f32_f16_sdwa v20, v20 dst_sel:DWORD dst_unused:UNUSED_PAD src0_sel:WORD_1
	v_pk_add_f32 v[28:29], v[28:29], v[54:55]
	v_mov_b32_e32 v19, v26
	v_pk_add_f32 v[54:55], v[24:25], v[26:27]
	v_pk_add_f32 v[26:27], v[36:37], v[50:51]
	v_pk_mov_b32 v[36:37], v[40:41], v[2:3] op_sel:[1,0]
	v_mov_b32_e32 v40, v45
	v_mov_b32_e32 v41, v18
	v_pk_add_f32 v[48:49], v[2:3], v[18:19]
	v_pk_add_f32 v[18:19], v[36:37], v[40:41]
	v_mov_b32_e32 v23, v52
	v_mov_b32_e32 v53, v51
	v_cvt_f32_f16_sdwa v57, v21 dst_sel:DWORD dst_unused:UNUSED_PAD src0_sel:WORD_1
	v_cvt_f32_f16_e32 v56, v21
	v_pk_add_f32 v[40:41], v[22:23], v[18:19]
	v_pk_add_f32 v[36:37], v[48:49], v[52:53]
	v_mov_b32_e32 v18, v51
	v_mov_b32_e32 v19, v55
	v_mov_b32_e32 v21, v41
	v_pk_add_f32 v[42:43], v[42:43], v[46:47]
	v_pk_add_f32 v[44:45], v[54:55], v[18:19]
	v_pk_mul_f32 v[18:19], v[54:55], v[54:55]
	v_pk_add_f32 v[48:49], v[40:41], v[20:21]
	v_pk_add_f32 v[20:21], v[26:27], v[36:37]
	v_pk_mul_f32 v[26:27], v[26:27], v[36:37]
	v_pk_add_f32 v[42:43], v[4:5], v[42:43]
	v_mov_b32_e32 v45, v19
	v_pk_mul_f32 v[18:19], v[40:41], v[40:41]
	v_mov_b32_e32 v21, v27
	v_pk_mul_f32 v[26:27], v[48:49], v[48:49]
	v_pk_add_f32 v[42:43], v[42:43], v[56:57]
	v_mov_b32_e32 v18, v48
	v_mov_b32_e32 v67, v26
	v_pk_mul_f32 v[38:39], v[28:29], v[28:29]
	v_pk_mul_f32 v[46:47], v[42:43], v[42:43]
	v_pk_add_f32 v[18:19], v[44:45], v[18:19]
	v_pk_add_f32 v[20:21], v[20:21], v[66:67]
	v_mov_b32_e32 v26, v42
	v_pk_add_f32 v[18:19], v[18:19], v[20:21]
	v_mov_b32_e32 v20, v28
	v_mov_b32_e32 v21, v38
	v_mov_b32_e32 v27, v46
	v_pk_add_f32 v[20:21], v[20:21], v[26:27]
	v_mov_b32_e32 v38, v29
	v_mov_b32_e32 v46, v43
	v_pk_add_f32 v[18:19], v[18:19], v[20:21]
	v_pk_add_f32 v[20:21], v[38:39], v[46:47]
	v_or_b32_e32 v23, s14, v87
	v_pk_add_f32 v[18:19], v[18:19], v[20:21]
	ds_bpermute_b32 v20, v30, v18
	ds_bpermute_b32 v21, v30, v19
	v_mul_lo_u32 v25, v23, s30
	v_cvt_pk_f16_f32 v27, v28, v29
	v_cvt_pk_f16_f32 v29, v42, v43
	v_add_lshl_u32 v25, v31, v25, 1
	s_waitcnt lgkmcnt(0)
	v_pk_add_f32 v[18:19], v[18:19], v[20:21]
	ds_bpermute_b32 v20, v32, v18
	ds_bpermute_b32 v21, v32, v19
	v_cvt_pk_f16_f32 v26, v55, v44
	v_cvt_pk_f16_f32 v28, v41, v48
	buffer_store_dwordx4 v[26:29], v25, s[8:11], 0 offen sc1
	s_waitcnt lgkmcnt(0)
	v_pk_add_f32 v[18:19], v[18:19], v[20:21]
	ds_bpermute_b32 v20, v33, v18
	ds_bpermute_b32 v21, v33, v19
	s_waitcnt lgkmcnt(0)
	v_pk_add_f32 v[18:19], v[18:19], v[20:21]
	ds_bpermute_b32 v20, v34, v18
	ds_bpermute_b32 v21, v34, v19
	s_and_saveexec_b64 s[0:1], vcc
	s_cbranch_execz .LBB7_7
	s_waitcnt lgkmcnt(0)
	v_pk_add_f32 v[64:65], v[18:19], v[20:21]
	v_lshl_add_u32 v18, v23, 6, s2
	v_mov_b32_e32 v67, v66
	s_mov_b32 s18, s10
	s_mov_b32 s19, s11
	buffer_store_dwordx4 v[64:67], v18, s[16:19], 0 offen sc1
.LBB7_7:
	s_or_b64 exec, exec, s[0:1]
	v_add_u32_e32 v18, 0, v91
	v_add_u32_e32 v23, s28, v91
	s_waitcnt lgkmcnt(0)
	ds_read_b128 v[18:21], v18
	ds_read_b128 v[26:29], v23
	v_add_u32_e32 v23, 0, v92
	v_add_u32_e32 v25, s28, v92
	ds_read_b128 v[36:39], v23
	ds_read_b128 v[40:43], v25
	v_cvt_f32_f16_e32 v46, v14
	v_cvt_f32_f16_e32 v48, v16
	s_waitcnt lgkmcnt(2)
	v_add_f32_e32 v45, v18, v26
	v_cvt_f32_f16_sdwa v47, v14 dst_sel:DWORD dst_unused:UNUSED_PAD src0_sel:WORD_1
	v_pk_mov_b32 v[18:19], v[18:19], v[6:7] op_sel:[1,0]
	v_mov_b32_e32 v44, v27
	s_waitcnt lgkmcnt(0)
	v_add_f32_e32 v14, v36, v40
	v_pk_add_f32 v[18:19], v[18:19], v[44:45]
	v_cvt_f32_f16_sdwa v16, v16 dst_sel:DWORD dst_unused:UNUSED_PAD src0_sel:WORD_1
	v_cvt_f32_f16_sdwa v51, v15 dst_sel:DWORD dst_unused:UNUSED_PAD src0_sel:WORD_1
	v_cvt_f32_f16_e32 v50, v15
	v_mov_b32_e32 v15, v18
	v_pk_mov_b32 v[36:37], v[36:37], v[2:3] op_sel:[1,0]
	v_mov_b32_e32 v40, v41
	v_mov_b32_e32 v41, v14
	v_pk_mov_b32 v[26:27], v[44:45], v[18:19] op_sel:[1,0]
	v_pk_add_f32 v[44:45], v[2:3], v[14:15]
	v_mov_b32_e32 v25, v46
	v_pk_add_f32 v[14:15], v[36:37], v[40:41]
	v_mov_b32_e32 v23, v48
	v_mov_b32_e32 v49, v47
	v_cvt_f32_f16_sdwa v53, v17 dst_sel:DWORD dst_unused:UNUSED_PAD src0_sel:WORD_1
	v_cvt_f32_f16_e32 v52, v17
	v_pk_add_f32 v[26:27], v[6:7], v[26:27]
	v_pk_add_f32 v[18:19], v[24:25], v[18:19]
	v_pk_add_f32 v[40:41], v[22:23], v[14:15]
	v_pk_add_f32 v[26:27], v[26:27], v[46:47]
	v_pk_add_f32 v[36:37], v[44:45], v[48:49]
	v_mov_b32_e32 v14, v47
	v_mov_b32_e32 v15, v19
	v_mov_b32_e32 v17, v41
	v_pk_add_f32 v[20:21], v[20:21], v[28:29]
	v_pk_add_f32 v[38:39], v[38:39], v[42:43]
	v_pk_add_f32 v[44:45], v[18:19], v[14:15]
	v_pk_mul_f32 v[14:15], v[18:19], v[18:19]
	v_pk_add_f32 v[46:47], v[40:41], v[16:17]
	v_pk_add_f32 v[16:17], v[26:27], v[36:37]
	v_pk_mul_f32 v[26:27], v[26:27], v[36:37]
	v_pk_add_f32 v[20:21], v[8:9], v[20:21]
	v_pk_add_f32 v[38:39], v[4:5], v[38:39]
	v_mov_b32_e32 v45, v15
	v_pk_mul_f32 v[14:15], v[40:41], v[40:41]
	v_mov_b32_e32 v17, v27
	v_pk_mul_f32 v[26:27], v[46:47], v[46:47]
	v_pk_add_f32 v[20:21], v[20:21], v[50:51]
	v_pk_add_f32 v[38:39], v[38:39], v[52:53]
	v_mov_b32_e32 v14, v46
	v_mov_b32_e32 v67, v26
	v_pk_mul_f32 v[28:29], v[20:21], v[20:21]
	v_pk_mul_f32 v[42:43], v[38:39], v[38:39]
	v_pk_add_f32 v[14:15], v[44:45], v[14:15]
	v_pk_add_f32 v[16:17], v[16:17], v[66:67]
	v_mov_b32_e32 v26, v38
	v_pk_add_f32 v[14:15], v[14:15], v[16:17]
	v_mov_b32_e32 v16, v20
	v_mov_b32_e32 v17, v28
	v_mov_b32_e32 v27, v42
	v_pk_add_f32 v[16:17], v[16:17], v[26:27]
	v_mov_b32_e32 v28, v21
	v_mov_b32_e32 v42, v39
	v_pk_add_f32 v[14:15], v[14:15], v[16:17]
	v_pk_add_f32 v[16:17], v[28:29], v[42:43]
	v_or_b32_e32 v18, s14, v90
	v_pk_add_f32 v[14:15], v[14:15], v[16:17]
	ds_bpermute_b32 v16, v30, v14
	ds_bpermute_b32 v17, v30, v15
	v_cvt_pk_f16_f32 v27, v20, v21
	v_mul_lo_u32 v20, v18, s30
	v_cvt_pk_f16_f32 v29, v38, v39
	v_add_lshl_u32 v20, v31, v20, 1
	s_waitcnt lgkmcnt(0)
	v_pk_add_f32 v[14:15], v[14:15], v[16:17]
	ds_bpermute_b32 v16, v32, v14
	ds_bpermute_b32 v17, v32, v15
	v_cvt_pk_f16_f32 v26, v19, v44
	v_cvt_pk_f16_f32 v28, v41, v46
	buffer_store_dwordx4 v[26:29], v20, s[8:11], 0 offen sc1
	s_waitcnt lgkmcnt(0)
	v_pk_add_f32 v[14:15], v[14:15], v[16:17]
	ds_bpermute_b32 v16, v33, v14
	ds_bpermute_b32 v17, v33, v15
	s_waitcnt lgkmcnt(0)
	v_pk_add_f32 v[14:15], v[14:15], v[16:17]
	ds_bpermute_b32 v16, v34, v14
	ds_bpermute_b32 v17, v34, v15
	s_and_saveexec_b64 s[0:1], vcc
	s_cbranch_execz .LBB7_9
	s_waitcnt lgkmcnt(0)
	v_pk_add_f32 v[64:65], v[14:15], v[16:17]
	v_lshl_add_u32 v14, v18, 6, s2
	v_mov_b32_e32 v67, v66
	s_mov_b32 s18, s10
	s_mov_b32 s19, s11
	buffer_store_dwordx4 v[64:67], v14, s[16:19], 0 offen sc1
.LBB7_9:
	s_or_b64 exec, exec, s[0:1]
	v_add_u32_e32 v14, 0, v94
	v_add_u32_e32 v18, s28, v94
	s_waitcnt lgkmcnt(0)
	ds_read_b128 v[14:17], v14
	ds_read_b128 v[18:21], v18
	v_add_u32_e32 v23, 0, v95
	v_add_u32_e32 v25, s28, v95
	ds_read_b128 v[26:29], v23
	ds_read_b128 v[36:39], v25
	v_cvt_f32_f16_e32 v42, v10
	s_waitcnt lgkmcnt(2)
	v_add_f32_e32 v41, v14, v18
	v_cvt_f32_f16_sdwa v43, v10 dst_sel:DWORD dst_unused:UNUSED_PAD src0_sel:WORD_1
	v_cvt_f32_f16_e32 v44, v12
	v_pk_mov_b32 v[14:15], v[14:15], v[6:7] op_sel:[1,0]
	v_mov_b32_e32 v40, v19
	v_pk_add_f32 v[14:15], v[14:15], v[40:41]
	s_waitcnt lgkmcnt(0)
	v_add_f32_e32 v10, v26, v36
	v_cvt_f32_f16_sdwa v47, v11 dst_sel:DWORD dst_unused:UNUSED_PAD src0_sel:WORD_1
	v_cvt_f32_f16_e32 v46, v11
	v_pk_mov_b32 v[18:19], v[40:41], v[14:15] op_sel:[1,0]
	v_mov_b32_e32 v11, v14
	v_mov_b32_e32 v25, v42
	v_cvt_f32_f16_sdwa v12, v12 dst_sel:DWORD dst_unused:UNUSED_PAD src0_sel:WORD_1
	v_pk_add_f32 v[6:7], v[6:7], v[18:19]
	v_pk_add_f32 v[18:19], v[2:3], v[10:11]
	v_pk_add_f32 v[14:15], v[24:25], v[14:15]
	v_pk_mov_b32 v[2:3], v[26:27], v[2:3] op_sel:[1,0]
	v_mov_b32_e32 v24, v37
	v_mov_b32_e32 v25, v10
	v_mov_b32_e32 v45, v43
	v_pk_add_f32 v[2:3], v[2:3], v[24:25]
	v_mov_b32_e32 v23, v44
	v_cvt_f32_f16_sdwa v49, v13 dst_sel:DWORD dst_unused:UNUSED_PAD src0_sel:WORD_1
	v_cvt_f32_f16_e32 v48, v13
	v_pk_add_f32 v[10:11], v[18:19], v[44:45]
	v_pk_add_f32 v[18:19], v[22:23], v[2:3]
	v_pk_add_f32 v[6:7], v[6:7], v[42:43]
	v_mov_b32_e32 v2, v43
	v_mov_b32_e32 v3, v15
	v_mov_b32_e32 v13, v19
	v_pk_add_f32 v[16:17], v[16:17], v[20:21]
	v_pk_add_f32 v[20:21], v[28:29], v[38:39]
	v_pk_add_f32 v[22:23], v[14:15], v[2:3]
	v_pk_mul_f32 v[2:3], v[14:15], v[14:15]
	v_pk_add_f32 v[12:13], v[18:19], v[12:13]
	v_pk_add_f32 v[24:25], v[6:7], v[10:11]
	v_pk_mul_f32 v[6:7], v[6:7], v[10:11]
	v_pk_add_f32 v[8:9], v[8:9], v[16:17]
	v_pk_add_f32 v[4:5], v[4:5], v[20:21]
	v_mov_b32_e32 v23, v3
	v_pk_mul_f32 v[2:3], v[18:19], v[18:19]
	v_mov_b32_e32 v25, v7
	v_pk_mul_f32 v[6:7], v[12:13], v[12:13]
	v_pk_add_f32 v[8:9], v[8:9], v[46:47]
	v_pk_add_f32 v[4:5], v[4:5], v[48:49]
	v_mov_b32_e32 v2, v12
	v_mov_b32_e32 v67, v6
	v_pk_mul_f32 v[16:17], v[8:9], v[8:9]
	v_pk_mul_f32 v[20:21], v[4:5], v[4:5]
	v_pk_add_f32 v[2:3], v[22:23], v[2:3]
	v_pk_add_f32 v[6:7], v[24:25], v[66:67]
	v_mov_b32_e32 v10, v4
	v_pk_add_f32 v[2:3], v[2:3], v[6:7]
	v_mov_b32_e32 v6, v8
	v_mov_b32_e32 v7, v16
	v_mov_b32_e32 v11, v20
	v_pk_add_f32 v[6:7], v[6:7], v[10:11]
	v_mov_b32_e32 v16, v9
	v_mov_b32_e32 v20, v5
	v_pk_add_f32 v[2:3], v[2:3], v[6:7]
	v_pk_add_f32 v[6:7], v[16:17], v[20:21]
	v_cvt_pk_f16_f32 v11, v4, v5
	v_pk_add_f32 v[2:3], v[2:3], v[6:7]
	ds_bpermute_b32 v6, v30, v2
	ds_bpermute_b32 v7, v30, v3
	v_cvt_pk_f16_f32 v9, v8, v9
	v_cvt_pk_f16_f32 v8, v15, v22
	v_cvt_pk_f16_f32 v10, v19, v12
	s_waitcnt lgkmcnt(0)
	v_pk_add_f32 v[2:3], v[2:3], v[6:7]
	ds_bpermute_b32 v6, v32, v2
	ds_bpermute_b32 v7, v32, v3
	s_waitcnt lgkmcnt(0)
	v_pk_add_f32 v[2:3], v[2:3], v[6:7]
	ds_bpermute_b32 v16, v33, v2
	ds_bpermute_b32 v17, v33, v3
	v_add_u32_e32 v6, s14, v93
	v_mul_lo_u32 v7, v6, s30
	v_add_lshl_u32 v7, v31, v7, 1
	buffer_store_dwordx4 v[8:11], v7, s[8:11], 0 offen sc1
	s_waitcnt lgkmcnt(0)
	v_pk_add_f32 v[2:3], v[2:3], v[16:17]
	ds_bpermute_b32 v4, v34, v2
	ds_bpermute_b32 v5, v34, v3
	s_and_saveexec_b64 s[0:1], vcc
	s_cbranch_execz .LBB7_2
	s_waitcnt lgkmcnt(0)
	v_pk_add_f32 v[64:65], v[2:3], v[4:5]
	v_lshl_add_u32 v2, v6, 6, s2
	v_mov_b32_e32 v67, v66
	s_mov_b32 s18, s10
	s_mov_b32 s19, s11
	buffer_store_dwordx4 v[64:67], v2, s[16:19], 0 offen sc1
	s_branch .LBB7_2

	.amdhsa_kernel _Z6gemm_pILi2ELi8EEvPKDF16_S1_iiiiiiPKfS3_S3_PfPDF16_S4_S5_S4_
		.amdhsa_group_segment_fixed_size 0
		.amdhsa_private_segment_fixed_size 0
		.amdhsa_kernarg_size 360
		.amdhsa_user_sgpr_count 2
		.amdhsa_user_sgpr_dispatch_ptr 0
		.amdhsa_user_sgpr_queue_ptr 0
		.amdhsa_user_sgpr_kernarg_segment_ptr 1
		.amdhsa_user_sgpr_dispatch_id 0
		.amdhsa_user_sgpr_kernarg_preload_length 0
		.amdhsa_user_sgpr_kernarg_preload_offset 0
		.amdhsa_user_sgpr_private_segment_size 0
		.amdhsa_uses_dynamic_stack 0
		.amdhsa_enable_private_segment 0
		.amdhsa_system_sgpr_workgroup_id_x 1
		.amdhsa_system_sgpr_workgroup_id_y 0
		.amdhsa_system_sgpr_workgroup_id_z 0
		.amdhsa_system_sgpr_workgroup_info 0
		.amdhsa_system_vgpr_workitem_id 0
		.amdhsa_next_free_vgpr 192
		.amdhsa_next_free_sgpr 52
		.amdhsa_accum_offset 192
		.amdhsa_reserve_vcc 1
		.amdhsa_float_round_mode_32 0
		.amdhsa_float_round_mode_16_64 0
		.amdhsa_float_denorm_mode_32 3
		.amdhsa_float_denorm_mode_16_64 3
		.amdhsa_dx10_clamp 1
		.amdhsa_ieee_mode 1
		.amdhsa_fp16_overflow 0
		.amdhsa_tg_split 0
		.amdhsa_exception_fp_ieee_invalid_op 0
		.amdhsa_exception_fp_denorm_src 0
		.amdhsa_exception_fp_ieee_div_zero 0
		.amdhsa_exception_fp_ieee_overflow 0
		.amdhsa_exception_fp_ieee_underflow 0
		.amdhsa_exception_fp_ieee_inexact 0
		.amdhsa_exception_int_div_zero 0
	.end_amdhsa_kernel

.LBB9_3:
	s_ashr_i32 s44, s23, 31
	s_xor_b32 s44, s44, s25
	s_abs_i32 s45, s23
	s_mul_hi_u32 s48, s45, s26
	s_mul_i32 s49, s48, s24
	s_sub_i32 s45, s45, s49
	s_add_i32 s49, s48, 1
	s_sub_i32 s46, s45, s24
	s_cmp_ge_u32 s45, s24
	s_cselect_b32 s48, s49, s48
	s_cselect_b32 s45, s46, s45
	s_add_i32 s49, s48, 1
	s_cmp_ge_u32 s45, s24
	s_cselect_b32 s45, s49, s48
	s_xor_b32 s45, s45, s44
	s_sub_i32 s44, s45, s44
	s_mul_i32 s45, s44, s21
	s_sub_i32 s47, s23, s45
	s_lshl_b32 s48, s47, 7
	s_lshl_b32 s46, s44, 7
	s_ashr_i32 s49, s48, 31
	v_or_b32_e32 v152, s46, v1
	v_lshl_add_u64 v[154:155], s[48:49], 1, v[70:71]
	v_mad_i64_i32 v[156:157], s[50:51], v152, s29, v[154:155]
	v_lshl_add_u64 v[158:159], s[48:49], 2, v[68:69]
	v_or_b32_e32 v153, 32, v152
	global_load_dwordx4 v[160:163], v[156:157], off
	v_mad_i64_i32 v[184:185], s[50:51], v153, s29, v[154:155]
	v_or_b32_e32 v153, 64, v152
	global_load_dwordx4 v[176:179], v[158:159], off
	global_load_dwordx4 v[180:183], v[158:159], off offset:16
	v_mad_i64_i32 v[186:187], s[50:51], v153, s29, v[154:155]
	v_or_b32_e32 v153, 0x60, v152
	global_load_dwordx4 v[164:167], v[184:185], off
	v_mad_i64_i32 v[188:189], s[50:51], v153, s29, v[154:155]
	global_load_dwordx4 v[168:171], v[186:187], off
	s_nop 0
	global_load_dwordx4 v[172:175], v[188:189], off
	v_add_u32_e32 v110, v80, v76
	s_waitcnt vmcnt(14)
	s_barrier
	s_waitcnt lgkmcnt(0)
	ds_read_b128 v[2:5], v110 offset:16384
	v_add_u32_e32 v111, v79, v76
	ds_read_b128 v[6:9], v111
	ds_read_b128 v[10:13], v111 offset:4096
	ds_read_b128 v[14:17], v110 offset:20480
	v_add_u32_e32 v67, v80, v77
	ds_read_b128 v[34:37], v67 offset:16384
	v_add_u32_e32 v109, v79, v77
	s_waitcnt lgkmcnt(3)
	v_mfma_f32_32x32x16_f16 v[50:65], v[2:5], v[6:9], 0
	ds_read_b128 v[112:115], v109
	ds_read_b128 v[116:119], v109 offset:4096
	ds_read_b128 v[120:123], v67 offset:20480
	v_readfirstlane_b32 s2, v0
	s_lshl_b32 s35, s27, 15
	s_lshl_b32 s2, s2, 4
	s_add_i32 s1, s35, 0
	s_and_b32 s39, s2, 0xfffffc00
	s_add_i32 s1, s1, s39
	s_waitcnt lgkmcnt(5)
	v_mfma_f32_32x32x16_f16 v[18:33], v[2:5], v[10:13], 0
	s_mov_b32 m0, s1
	s_add_i32 s2, s1, 0x2000
	buffer_load_dwordx4 v72, s[4:7], s0 offen lds
	s_mov_b32 m0, s2
	s_add_i32 s3, s1, 0x4000
	buffer_load_dwordx4 v74, s[4:7], s0 offen lds
	s_mov_b32 s14, s10
	s_waitcnt lgkmcnt(2)
	v_mfma_f32_32x32x16_f16 v[50:65], v[34:37], v[112:115], v[50:65]
	s_mov_b32 s15, s11
	s_mov_b32 m0, s3
	s_add_i32 s18, s1, 0x6000
	buffer_load_dwordx4 v73, s[12:15], s0 offen lds
	s_mov_b32 m0, s18
	s_add_i32 s19, s35, 0x8000
	buffer_load_dwordx4 v75, s[12:15], s0 offen lds
	s_waitcnt lgkmcnt(1)
	v_mfma_f32_32x32x16_f16 v[18:33], v[34:37], v[116:119], v[18:33]
	s_waitcnt vmcnt(14)
	s_barrier
	s_and_b32 s19, s19, 0x18000
	s_add_i32 s19, s19, 0
	s_add_i32 s19, s19, s39
	s_add_i32 s36, s0, 0x80
	s_mov_b32 m0, s19
	v_mfma_f32_32x32x16_f16 v[34:49], v[14:17], v[6:9], 0
	s_add_i32 s31, s19, 0x2000
	s_add_i32 s33, s19, 0x4000
	s_add_i32 s34, s19, 0x6000
	s_xor_b32 s40, s35, 0x10000
	s_add_i32 s35, s40, 0
	s_add_i32 s35, s35, s39
	s_add_i32 s41, s0, 0x100
	v_mfma_f32_32x32x16_f16 v[2:17], v[14:17], v[10:13], 0
	s_add_i32 s37, s35, 0x4000
	s_add_i32 s38, s35, 0x6000
	s_add_i32 s40, s40, 0x8000
	s_and_b32 s40, s40, 0x18000
	s_add_i32 s40, s40, 0
	s_add_i32 s39, s40, s39
	s_add_i32 s43, s0, 0x180
	s_waitcnt lgkmcnt(0)
	v_mfma_f32_32x32x16_f16 v[34:49], v[120:123], v[112:115], v[34:49]
	s_add_i32 s40, s39, 0x2000
	s_add_i32 s42, s39, 0x6000
	v_mfma_f32_32x32x16_f16 v[2:17], v[120:123], v[116:119], v[2:17]
	ds_read_b128 v[112:115], v110 offset:49152
	ds_read_b128 v[116:119], v111 offset:32768
	ds_read_b128 v[120:123], v111 offset:36864
	ds_read_b128 v[124:127], v110 offset:53248
	s_waitcnt lgkmcnt(2)
	v_mfma_f32_32x32x16_f16 v[50:65], v[112:115], v[116:119], v[50:65]
	s_waitcnt lgkmcnt(1)
	v_mfma_f32_32x32x16_f16 v[18:33], v[112:115], v[120:123], v[18:33]
	s_waitcnt lgkmcnt(0)
	v_mfma_f32_32x32x16_f16 v[34:49], v[124:127], v[116:119], v[34:49]
	v_mfma_f32_32x32x16_f16 v[2:17], v[124:127], v[120:123], v[2:17]
	ds_read_b128 v[112:115], v67 offset:49152
	ds_read_b128 v[116:119], v109 offset:32768
	ds_read_b128 v[120:123], v109 offset:36864
	ds_read_b128 v[124:127], v67 offset:53248
	buffer_load_dwordx4 v72, s[4:7], s36 offen lds
	s_mov_b32 m0, s31
	s_nop 0
	buffer_load_dwordx4 v74, s[4:7], s36 offen lds
	s_mov_b32 m0, s33
	s_nop 0
	buffer_load_dwordx4 v73, s[12:15], s36 offen lds
	s_mov_b32 m0, s34
	s_waitcnt lgkmcnt(2)
	v_mfma_f32_32x32x16_f16 v[50:65], v[112:115], v[116:119], v[50:65]
	buffer_load_dwordx4 v75, s[12:15], s36 offen lds
	s_waitcnt vmcnt(14)
	s_barrier
	s_mov_b32 m0, s35
	s_add_i32 s36, s35, 0x2000
	s_waitcnt lgkmcnt(1)
	v_mfma_f32_32x32x16_f16 v[18:33], v[112:115], v[120:123], v[18:33]
	v_add_u32_e32 v113, v81, v76
	v_add_u32_e32 v112, v82, v76
	s_waitcnt lgkmcnt(0)
	v_mfma_f32_32x32x16_f16 v[34:49], v[124:127], v[116:119], v[34:49]
	ds_read_b128 v[114:117], v96
	v_mfma_f32_32x32x16_f16 v[2:17], v[124:127], v[120:123], v[2:17]
	ds_read_b128 v[118:121], v113
	ds_read_b128 v[122:125], v113 offset:4096
	ds_read_b128 v[126:129], v112 offset:4096
	s_waitcnt lgkmcnt(2)
	v_mfma_f32_32x32x16_f16 v[50:65], v[114:117], v[118:121], v[50:65]
	s_waitcnt lgkmcnt(1)
	v_mfma_f32_32x32x16_f16 v[18:33], v[114:117], v[122:125], v[18:33]
	v_add_u32_e32 v115, v81, v77
	v_add_u32_e32 v114, v82, v77
	s_waitcnt lgkmcnt(0)
	v_mfma_f32_32x32x16_f16 v[34:49], v[126:129], v[118:121], v[34:49]
	ds_read_b128 v[116:119], v97
	v_mfma_f32_32x32x16_f16 v[2:17], v[126:129], v[122:125], v[2:17]
	ds_read_b128 v[120:123], v115
	ds_read_b128 v[124:127], v115 offset:4096
	ds_read_b128 v[128:131], v114 offset:4096
	buffer_load_dwordx4 v72, s[4:7], s41 offen lds
	s_mov_b32 m0, s36
	s_nop 0
	buffer_load_dwordx4 v74, s[4:7], s41 offen lds
	s_mov_b32 m0, s37
	s_waitcnt lgkmcnt(2)
	v_mfma_f32_32x32x16_f16 v[50:65], v[116:119], v[120:123], v[50:65]
	buffer_load_dwordx4 v73, s[12:15], s41 offen lds
	s_mov_b32 m0, s38
	s_nop 0
	buffer_load_dwordx4 v75, s[12:15], s41 offen lds
	s_waitcnt vmcnt(8)
	s_barrier
	s_mov_b32 m0, s39
	s_waitcnt lgkmcnt(1)
	v_mfma_f32_32x32x16_f16 v[18:33], v[116:119], v[124:127], v[18:33]
	v_add_u32_e32 v117, v83, v76
	v_add_u32_e32 v116, v84, v76
	s_add_i32 s41, s39, 0x4000
	s_waitcnt lgkmcnt(0)
	v_mfma_f32_32x32x16_f16 v[34:49], v[128:131], v[120:123], v[34:49]
	ds_read_b128 v[118:121], v98
	v_mfma_f32_32x32x16_f16 v[2:17], v[128:131], v[124:127], v[2:17]
	ds_read_b128 v[122:125], v117
	ds_read_b128 v[126:129], v117 offset:4096
	ds_read_b128 v[130:133], v116 offset:4096
	s_waitcnt lgkmcnt(2)
	v_mfma_f32_32x32x16_f16 v[50:65], v[118:121], v[122:125], v[50:65]
	s_waitcnt lgkmcnt(1)
	v_mfma_f32_32x32x16_f16 v[18:33], v[118:121], v[126:129], v[18:33]
	v_add_u32_e32 v119, v83, v77
	v_add_u32_e32 v118, v84, v77
	s_waitcnt lgkmcnt(0)
	v_mfma_f32_32x32x16_f16 v[34:49], v[130:133], v[122:125], v[34:49]
	ds_read_b128 v[120:123], v99
	v_mfma_f32_32x32x16_f16 v[2:17], v[130:133], v[126:129], v[2:17]
	ds_read_b128 v[124:127], v119
	ds_read_b128 v[128:131], v119 offset:4096
	ds_read_b128 v[132:135], v118 offset:4096
	buffer_load_dwordx4 v72, s[4:7], s43 offen lds
	s_mov_b32 m0, s40
	s_nop 0
	buffer_load_dwordx4 v74, s[4:7], s43 offen lds
	s_mov_b32 m0, s41
	s_waitcnt lgkmcnt(2)
	v_mfma_f32_32x32x16_f16 v[50:65], v[120:123], v[124:127], v[50:65]
	buffer_load_dwordx4 v73, s[12:15], s43 offen lds
	s_mov_b32 m0, s42
	s_nop 0
	buffer_load_dwordx4 v75, s[12:15], s43 offen lds
	s_waitcnt vmcnt(8)
	s_barrier
	s_add_i32 s43, s0, 0x200
	s_waitcnt lgkmcnt(1)
	v_mfma_f32_32x32x16_f16 v[18:33], v[120:123], v[128:131], v[18:33]
	s_mov_b32 m0, s1
	s_waitcnt lgkmcnt(0)
	v_mfma_f32_32x32x16_f16 v[34:49], v[132:135], v[124:127], v[34:49]
	v_mfma_f32_32x32x16_f16 v[2:17], v[132:135], v[128:131], v[2:17]
	ds_read_b128 v[120:123], v110 offset:16384
	ds_read_b128 v[124:127], v111
	ds_read_b128 v[128:131], v111 offset:4096
	ds_read_b128 v[132:135], v110 offset:20480
	s_waitcnt lgkmcnt(2)
	v_mfma_f32_32x32x16_f16 v[50:65], v[120:123], v[124:127], v[50:65]
	s_waitcnt lgkmcnt(1)
	v_mfma_f32_32x32x16_f16 v[18:33], v[120:123], v[128:131], v[18:33]
	s_waitcnt lgkmcnt(0)
	v_mfma_f32_32x32x16_f16 v[34:49], v[132:135], v[124:127], v[34:49]
	v_mfma_f32_32x32x16_f16 v[2:17], v[132:135], v[128:131], v[2:17]
	ds_read_b128 v[120:123], v67 offset:16384
	ds_read_b128 v[124:127], v109
	ds_read_b128 v[128:131], v109 offset:4096
	ds_read_b128 v[132:135], v67 offset:20480
	buffer_load_dwordx4 v72, s[4:7], s43 offen lds
	s_mov_b32 m0, s2
	s_nop 0
	buffer_load_dwordx4 v74, s[4:7], s43 offen lds
	s_mov_b32 m0, s3
	s_waitcnt lgkmcnt(2)
	v_mfma_f32_32x32x16_f16 v[50:65], v[120:123], v[124:127], v[50:65]
	buffer_load_dwordx4 v73, s[12:15], s43 offen lds
	s_mov_b32 m0, s18
	s_nop 0
	buffer_load_dwordx4 v75, s[12:15], s43 offen lds
	s_waitcnt vmcnt(8)
	s_barrier
	s_add_i32 s43, s0, 0x280
	s_waitcnt lgkmcnt(1)
	v_mfma_f32_32x32x16_f16 v[18:33], v[120:123], v[128:131], v[18:33]
	s_mov_b32 m0, s19
	s_waitcnt lgkmcnt(0)
	v_mfma_f32_32x32x16_f16 v[34:49], v[132:135], v[124:127], v[34:49]
	v_mfma_f32_32x32x16_f16 v[2:17], v[132:135], v[128:131], v[2:17]
	ds_read_b128 v[120:123], v110 offset:49152
	ds_read_b128 v[124:127], v111 offset:32768
	ds_read_b128 v[128:131], v111 offset:36864
	ds_read_b128 v[132:135], v110 offset:53248
	s_waitcnt lgkmcnt(2)
	v_mfma_f32_32x32x16_f16 v[50:65], v[120:123], v[124:127], v[50:65]
	s_waitcnt lgkmcnt(1)
	v_mfma_f32_32x32x16_f16 v[18:33], v[120:123], v[128:131], v[18:33]
	s_waitcnt lgkmcnt(0)
	v_mfma_f32_32x32x16_f16 v[34:49], v[132:135], v[124:127], v[34:49]
	v_mfma_f32_32x32x16_f16 v[2:17], v[132:135], v[128:131], v[2:17]
	ds_read_b128 v[120:123], v67 offset:49152
	ds_read_b128 v[124:127], v109 offset:32768
	ds_read_b128 v[128:131], v109 offset:36864
	ds_read_b128 v[132:135], v67 offset:53248
	buffer_load_dwordx4 v72, s[4:7], s43 offen lds
	s_mov_b32 m0, s31
	s_nop 0
	buffer_load_dwordx4 v74, s[4:7], s43 offen lds
	s_mov_b32 m0, s33
	s_waitcnt lgkmcnt(2)
	v_mfma_f32_32x32x16_f16 v[50:65], v[120:123], v[124:127], v[50:65]
	buffer_load_dwordx4 v73, s[12:15], s43 offen lds
	s_mov_b32 m0, s34
	s_nop 0
	buffer_load_dwordx4 v75, s[12:15], s43 offen lds
	s_waitcnt vmcnt(8)
	s_barrier
	s_add_i32 s43, s0, 0x300
	s_waitcnt lgkmcnt(1)
	v_mfma_f32_32x32x16_f16 v[18:33], v[120:123], v[128:131], v[18:33]
	s_mov_b32 m0, s35
	s_waitcnt lgkmcnt(0)
	v_mfma_f32_32x32x16_f16 v[34:49], v[132:135], v[124:127], v[34:49]
	v_mfma_f32_32x32x16_f16 v[2:17], v[132:135], v[128:131], v[2:17]
	ds_read_b128 v[120:123], v96
	ds_read_b128 v[124:127], v113
	ds_read_b128 v[128:131], v113 offset:4096
	ds_read_b128 v[132:135], v112 offset:4096
	s_waitcnt lgkmcnt(2)
	v_mfma_f32_32x32x16_f16 v[50:65], v[120:123], v[124:127], v[50:65]
	s_waitcnt lgkmcnt(1)
	v_mfma_f32_32x32x16_f16 v[18:33], v[120:123], v[128:131], v[18:33]
	s_waitcnt lgkmcnt(0)
	v_mfma_f32_32x32x16_f16 v[34:49], v[132:135], v[124:127], v[34:49]
	v_mfma_f32_32x32x16_f16 v[2:17], v[132:135], v[128:131], v[2:17]
	ds_read_b128 v[120:123], v97
	ds_read_b128 v[124:127], v115
	ds_read_b128 v[128:131], v115 offset:4096
	ds_read_b128 v[132:135], v114 offset:4096
	buffer_load_dwordx4 v72, s[4:7], s43 offen lds
	s_mov_b32 m0, s36
	s_nop 0
	buffer_load_dwordx4 v74, s[4:7], s43 offen lds
	s_mov_b32 m0, s37
	s_waitcnt lgkmcnt(2)
	v_mfma_f32_32x32x16_f16 v[50:65], v[120:123], v[124:127], v[50:65]
	buffer_load_dwordx4 v73, s[12:15], s43 offen lds
	s_mov_b32 m0, s38
	s_nop 0
	buffer_load_dwordx4 v75, s[12:15], s43 offen lds
	s_waitcnt vmcnt(8)
	s_barrier
	s_add_i32 s43, s0, 0x380
	s_waitcnt lgkmcnt(1)
	v_mfma_f32_32x32x16_f16 v[18:33], v[120:123], v[128:131], v[18:33]
	s_mov_b32 m0, s39
	s_waitcnt lgkmcnt(0)
	v_mfma_f32_32x32x16_f16 v[34:49], v[132:135], v[124:127], v[34:49]
	v_mfma_f32_32x32x16_f16 v[2:17], v[132:135], v[128:131], v[2:17]
	ds_read_b128 v[120:123], v98
	ds_read_b128 v[124:127], v117
	ds_read_b128 v[128:131], v117 offset:4096
	ds_read_b128 v[132:135], v116 offset:4096
	s_waitcnt lgkmcnt(2)
	v_mfma_f32_32x32x16_f16 v[50:65], v[120:123], v[124:127], v[50:65]
	s_waitcnt lgkmcnt(1)
	v_mfma_f32_32x32x16_f16 v[18:33], v[120:123], v[128:131], v[18:33]
	s_waitcnt lgkmcnt(0)
	v_mfma_f32_32x32x16_f16 v[34:49], v[132:135], v[124:127], v[34:49]
	v_mfma_f32_32x32x16_f16 v[2:17], v[132:135], v[128:131], v[2:17]
	ds_read_b128 v[120:123], v99
	ds_read_b128 v[124:127], v119
	ds_read_b128 v[128:131], v119 offset:4096
	ds_read_b128 v[132:135], v118 offset:4096
	buffer_load_dwordx4 v72, s[4:7], s43 offen lds
	s_mov_b32 m0, s40
	s_nop 0
	buffer_load_dwordx4 v74, s[4:7], s43 offen lds
	s_mov_b32 m0, s41
	s_waitcnt lgkmcnt(2)
	v_mfma_f32_32x32x16_f16 v[50:65], v[120:123], v[124:127], v[50:65]
	buffer_load_dwordx4 v73, s[12:15], s43 offen lds
	s_mov_b32 m0, s42
	s_nop 0
	buffer_load_dwordx4 v75, s[12:15], s43 offen lds
	s_waitcnt vmcnt(8)
	s_barrier
	s_add_i32 s43, s0, 0x400
	s_waitcnt lgkmcnt(1)
	v_mfma_f32_32x32x16_f16 v[18:33], v[120:123], v[128:131], v[18:33]
	s_mov_b32 m0, s1
	s_waitcnt lgkmcnt(0)
	v_mfma_f32_32x32x16_f16 v[34:49], v[132:135], v[124:127], v[34:49]
	v_mfma_f32_32x32x16_f16 v[2:17], v[132:135], v[128:131], v[2:17]
	ds_read_b128 v[120:123], v110 offset:16384
	ds_read_b128 v[124:127], v111
	ds_read_b128 v[128:131], v111 offset:4096
	ds_read_b128 v[132:135], v110 offset:20480
	s_waitcnt lgkmcnt(2)
	v_mfma_f32_32x32x16_f16 v[50:65], v[120:123], v[124:127], v[50:65]
	s_waitcnt lgkmcnt(1)
	v_mfma_f32_32x32x16_f16 v[18:33], v[120:123], v[128:131], v[18:33]
	s_waitcnt lgkmcnt(0)
	v_mfma_f32_32x32x16_f16 v[34:49], v[132:135], v[124:127], v[34:49]
	v_mfma_f32_32x32x16_f16 v[2:17], v[132:135], v[128:131], v[2:17]
	ds_read_b128 v[120:123], v67 offset:16384
	ds_read_b128 v[124:127], v109
	ds_read_b128 v[128:131], v109 offset:4096
	ds_read_b128 v[132:135], v67 offset:20480
	buffer_load_dwordx4 v72, s[4:7], s43 offen lds
	s_mov_b32 m0, s2
	s_nop 0
	buffer_load_dwordx4 v74, s[4:7], s43 offen lds
	s_mov_b32 m0, s3
	s_waitcnt lgkmcnt(2)
	v_mfma_f32_32x32x16_f16 v[50:65], v[120:123], v[124:127], v[50:65]
	buffer_load_dwordx4 v73, s[12:15], s43 offen lds
	s_mov_b32 m0, s18
	s_nop 0
	buffer_load_dwordx4 v75, s[12:15], s43 offen lds
	s_waitcnt vmcnt(8)
	s_barrier
	s_add_i32 s43, s0, 0x480
	s_waitcnt lgkmcnt(1)
	v_mfma_f32_32x32x16_f16 v[18:33], v[120:123], v[128:131], v[18:33]
	s_mov_b32 m0, s19
	s_waitcnt lgkmcnt(0)
	v_mfma_f32_32x32x16_f16 v[34:49], v[132:135], v[124:127], v[34:49]
	v_mfma_f32_32x32x16_f16 v[2:17], v[132:135], v[128:131], v[2:17]
	ds_read_b128 v[120:123], v110 offset:49152
	ds_read_b128 v[124:127], v111 offset:32768
	ds_read_b128 v[128:131], v111 offset:36864
	ds_read_b128 v[132:135], v110 offset:53248
	s_waitcnt lgkmcnt(2)
	v_mfma_f32_32x32x16_f16 v[50:65], v[120:123], v[124:127], v[50:65]
	s_waitcnt lgkmcnt(1)
	v_mfma_f32_32x32x16_f16 v[18:33], v[120:123], v[128:131], v[18:33]
	s_waitcnt lgkmcnt(0)
	v_mfma_f32_32x32x16_f16 v[34:49], v[132:135], v[124:127], v[34:49]
	v_mfma_f32_32x32x16_f16 v[2:17], v[132:135], v[128:131], v[2:17]
	ds_read_b128 v[120:123], v67 offset:49152
	ds_read_b128 v[124:127], v109 offset:32768
	ds_read_b128 v[128:131], v109 offset:36864
	ds_read_b128 v[132:135], v67 offset:53248
	buffer_load_dwordx4 v72, s[4:7], s43 offen lds
	s_mov_b32 m0, s31
	s_nop 0
	buffer_load_dwordx4 v74, s[4:7], s43 offen lds
	s_mov_b32 m0, s33
	s_waitcnt lgkmcnt(2)
	v_mfma_f32_32x32x16_f16 v[50:65], v[120:123], v[124:127], v[50:65]
	buffer_load_dwordx4 v73, s[12:15], s43 offen lds
	s_mov_b32 m0, s34
	s_nop 0
	buffer_load_dwordx4 v75, s[12:15], s43 offen lds
	s_waitcnt vmcnt(8)
	s_barrier
	s_add_i32 s43, s0, 0x500
	s_waitcnt lgkmcnt(1)
	v_mfma_f32_32x32x16_f16 v[18:33], v[120:123], v[128:131], v[18:33]
	s_mov_b32 m0, s35
	s_waitcnt lgkmcnt(0)
	v_mfma_f32_32x32x16_f16 v[34:49], v[132:135], v[124:127], v[34:49]
	v_mfma_f32_32x32x16_f16 v[2:17], v[132:135], v[128:131], v[2:17]
	ds_read_b128 v[120:123], v96
	ds_read_b128 v[124:127], v113
	ds_read_b128 v[128:131], v113 offset:4096
	ds_read_b128 v[132:135], v112 offset:4096
	s_waitcnt lgkmcnt(2)
	v_mfma_f32_32x32x16_f16 v[50:65], v[120:123], v[124:127], v[50:65]
	s_waitcnt lgkmcnt(1)
	v_mfma_f32_32x32x16_f16 v[18:33], v[120:123], v[128:131], v[18:33]
	s_waitcnt lgkmcnt(0)
	v_mfma_f32_32x32x16_f16 v[34:49], v[132:135], v[124:127], v[34:49]
	v_mfma_f32_32x32x16_f16 v[2:17], v[132:135], v[128:131], v[2:17]
	ds_read_b128 v[120:123], v97
	ds_read_b128 v[124:127], v115
	ds_read_b128 v[128:131], v115 offset:4096
	ds_read_b128 v[132:135], v114 offset:4096
	buffer_load_dwordx4 v72, s[4:7], s43 offen lds
	s_mov_b32 m0, s36
	s_nop 0
	buffer_load_dwordx4 v74, s[4:7], s43 offen lds
	s_mov_b32 m0, s37
	s_waitcnt lgkmcnt(2)
	v_mfma_f32_32x32x16_f16 v[50:65], v[120:123], v[124:127], v[50:65]
	buffer_load_dwordx4 v73, s[12:15], s43 offen lds
	s_mov_b32 m0, s38
	s_nop 0
	buffer_load_dwordx4 v75, s[12:15], s43 offen lds
	s_waitcnt vmcnt(8)
	s_barrier
	s_add_i32 s43, s0, 0x580
	s_waitcnt lgkmcnt(1)
	v_mfma_f32_32x32x16_f16 v[18:33], v[120:123], v[128:131], v[18:33]
	s_mov_b32 m0, s39
	s_waitcnt lgkmcnt(0)
	v_mfma_f32_32x32x16_f16 v[34:49], v[132:135], v[124:127], v[34:49]
	v_mfma_f32_32x32x16_f16 v[2:17], v[132:135], v[128:131], v[2:17]
	ds_read_b128 v[120:123], v98
	ds_read_b128 v[124:127], v117
	ds_read_b128 v[128:131], v117 offset:4096
	ds_read_b128 v[132:135], v116 offset:4096
	s_waitcnt lgkmcnt(2)
	v_mfma_f32_32x32x16_f16 v[50:65], v[120:123], v[124:127], v[50:65]
	s_waitcnt lgkmcnt(1)
	v_mfma_f32_32x32x16_f16 v[18:33], v[120:123], v[128:131], v[18:33]
	s_waitcnt lgkmcnt(0)
	v_mfma_f32_32x32x16_f16 v[34:49], v[132:135], v[124:127], v[34:49]
	v_mfma_f32_32x32x16_f16 v[2:17], v[132:135], v[128:131], v[2:17]
	ds_read_b128 v[120:123], v99
	ds_read_b128 v[124:127], v119
	ds_read_b128 v[128:131], v119 offset:4096
	ds_read_b128 v[132:135], v118 offset:4096
	buffer_load_dwordx4 v72, s[4:7], s43 offen lds
	s_mov_b32 m0, s40
	s_nop 0
	buffer_load_dwordx4 v74, s[4:7], s43 offen lds
	s_mov_b32 m0, s41
	s_waitcnt lgkmcnt(2)
	v_mfma_f32_32x32x16_f16 v[50:65], v[120:123], v[124:127], v[50:65]
	buffer_load_dwordx4 v73, s[12:15], s43 offen lds
	s_mov_b32 m0, s42
	s_nop 0
	buffer_load_dwordx4 v75, s[12:15], s43 offen lds
	s_waitcnt vmcnt(8)
	s_barrier
	s_add_i32 s43, s0, 0x600
	s_waitcnt lgkmcnt(1)
	v_mfma_f32_32x32x16_f16 v[18:33], v[120:123], v[128:131], v[18:33]
	s_mov_b32 m0, s1
	s_waitcnt lgkmcnt(0)
	v_mfma_f32_32x32x16_f16 v[34:49], v[132:135], v[124:127], v[34:49]
	v_mfma_f32_32x32x16_f16 v[2:17], v[132:135], v[128:131], v[2:17]
	ds_read_b128 v[120:123], v110 offset:16384
	ds_read_b128 v[124:127], v111
	ds_read_b128 v[128:131], v111 offset:4096
	ds_read_b128 v[132:135], v110 offset:20480
	s_waitcnt lgkmcnt(2)
	v_mfma_f32_32x32x16_f16 v[50:65], v[120:123], v[124:127], v[50:65]
	s_waitcnt lgkmcnt(1)
	v_mfma_f32_32x32x16_f16 v[18:33], v[120:123], v[128:131], v[18:33]
	s_waitcnt lgkmcnt(0)
	v_mfma_f32_32x32x16_f16 v[34:49], v[132:135], v[124:127], v[34:49]
	v_mfma_f32_32x32x16_f16 v[2:17], v[132:135], v[128:131], v[2:17]
	ds_read_b128 v[120:123], v67 offset:16384
	ds_read_b128 v[124:127], v109
	ds_read_b128 v[128:131], v109 offset:4096
	ds_read_b128 v[132:135], v67 offset:20480
	buffer_load_dwordx4 v72, s[4:7], s43 offen lds
	s_mov_b32 m0, s2
	s_nop 0
	buffer_load_dwordx4 v74, s[4:7], s43 offen lds
	s_mov_b32 m0, s3
	s_waitcnt lgkmcnt(2)
	v_mfma_f32_32x32x16_f16 v[50:65], v[120:123], v[124:127], v[50:65]
	buffer_load_dwordx4 v73, s[12:15], s43 offen lds
	s_mov_b32 m0, s18
	s_nop 0
	buffer_load_dwordx4 v75, s[12:15], s43 offen lds
	s_waitcnt vmcnt(8)
	s_barrier
	s_add_i32 s43, s0, 0x680
	s_waitcnt lgkmcnt(1)
	v_mfma_f32_32x32x16_f16 v[18:33], v[120:123], v[128:131], v[18:33]
	s_mov_b32 m0, s19
	s_waitcnt lgkmcnt(0)
	v_mfma_f32_32x32x16_f16 v[34:49], v[132:135], v[124:127], v[34:49]
	v_mfma_f32_32x32x16_f16 v[2:17], v[132:135], v[128:131], v[2:17]
	ds_read_b128 v[120:123], v110 offset:49152
	ds_read_b128 v[124:127], v111 offset:32768
	ds_read_b128 v[128:131], v111 offset:36864
	ds_read_b128 v[132:135], v110 offset:53248
	s_waitcnt lgkmcnt(2)
	v_mfma_f32_32x32x16_f16 v[50:65], v[120:123], v[124:127], v[50:65]
	s_waitcnt lgkmcnt(1)
	v_mfma_f32_32x32x16_f16 v[18:33], v[120:123], v[128:131], v[18:33]
	s_waitcnt lgkmcnt(0)
	v_mfma_f32_32x32x16_f16 v[34:49], v[132:135], v[124:127], v[34:49]
	v_mfma_f32_32x32x16_f16 v[2:17], v[132:135], v[128:131], v[2:17]
	ds_read_b128 v[120:123], v67 offset:49152
	ds_read_b128 v[124:127], v109 offset:32768
	ds_read_b128 v[128:131], v109 offset:36864
	ds_read_b128 v[132:135], v67 offset:53248
	buffer_load_dwordx4 v72, s[4:7], s43 offen lds
	s_mov_b32 m0, s31
	s_nop 0
	buffer_load_dwordx4 v74, s[4:7], s43 offen lds
	s_mov_b32 m0, s33
	s_waitcnt lgkmcnt(2)
	v_mfma_f32_32x32x16_f16 v[50:65], v[120:123], v[124:127], v[50:65]
	buffer_load_dwordx4 v73, s[12:15], s43 offen lds
	s_mov_b32 m0, s34
	s_nop 0
	buffer_load_dwordx4 v75, s[12:15], s43 offen lds
	s_waitcnt vmcnt(8)
	s_barrier
	s_add_i32 s43, s0, 0x700
	s_waitcnt lgkmcnt(1)
	v_mfma_f32_32x32x16_f16 v[18:33], v[120:123], v[128:131], v[18:33]
	s_mov_b32 m0, s35
	s_waitcnt lgkmcnt(0)
	v_mfma_f32_32x32x16_f16 v[34:49], v[132:135], v[124:127], v[34:49]
	v_mfma_f32_32x32x16_f16 v[2:17], v[132:135], v[128:131], v[2:17]
	ds_read_b128 v[120:123], v96
	ds_read_b128 v[124:127], v113
	ds_read_b128 v[128:131], v113 offset:4096
	ds_read_b128 v[132:135], v112 offset:4096
	s_waitcnt lgkmcnt(2)
	v_mfma_f32_32x32x16_f16 v[50:65], v[120:123], v[124:127], v[50:65]
	s_waitcnt lgkmcnt(1)
	v_mfma_f32_32x32x16_f16 v[18:33], v[120:123], v[128:131], v[18:33]
	s_waitcnt lgkmcnt(0)
	v_mfma_f32_32x32x16_f16 v[34:49], v[132:135], v[124:127], v[34:49]
	v_mfma_f32_32x32x16_f16 v[2:17], v[132:135], v[128:131], v[2:17]
	ds_read_b128 v[120:123], v97
	ds_read_b128 v[124:127], v115
	ds_read_b128 v[128:131], v115 offset:4096
	ds_read_b128 v[132:135], v114 offset:4096
	buffer_load_dwordx4 v72, s[4:7], s43 offen lds
	s_mov_b32 m0, s36
	s_nop 0
	buffer_load_dwordx4 v74, s[4:7], s43 offen lds
	s_mov_b32 m0, s37
	s_waitcnt lgkmcnt(2)
	v_mfma_f32_32x32x16_f16 v[50:65], v[120:123], v[124:127], v[50:65]
	buffer_load_dwordx4 v73, s[12:15], s43 offen lds
	s_mov_b32 m0, s38
	s_nop 0
	buffer_load_dwordx4 v75, s[12:15], s43 offen lds
	s_waitcnt vmcnt(8)
	s_barrier
	s_add_i32 s43, s0, 0x780
	s_waitcnt lgkmcnt(1)
	v_mfma_f32_32x32x16_f16 v[18:33], v[120:123], v[128:131], v[18:33]
	s_mov_b32 m0, s39
	s_waitcnt lgkmcnt(0)
	v_mfma_f32_32x32x16_f16 v[34:49], v[132:135], v[124:127], v[34:49]
	v_mfma_f32_32x32x16_f16 v[2:17], v[132:135], v[128:131], v[2:17]
	ds_read_b128 v[120:123], v98
	ds_read_b128 v[124:127], v117
	ds_read_b128 v[128:131], v117 offset:4096
	ds_read_b128 v[132:135], v116 offset:4096
	s_waitcnt lgkmcnt(2)
	v_mfma_f32_32x32x16_f16 v[50:65], v[120:123], v[124:127], v[50:65]
	s_waitcnt lgkmcnt(1)
	v_mfma_f32_32x32x16_f16 v[18:33], v[120:123], v[128:131], v[18:33]
	s_waitcnt lgkmcnt(0)
	v_mfma_f32_32x32x16_f16 v[34:49], v[132:135], v[124:127], v[34:49]
	v_mfma_f32_32x32x16_f16 v[2:17], v[132:135], v[128:131], v[2:17]
	ds_read_b128 v[120:123], v99
	ds_read_b128 v[124:127], v119
	ds_read_b128 v[128:131], v119 offset:4096
	ds_read_b128 v[132:135], v118 offset:4096
	buffer_load_dwordx4 v72, s[4:7], s43 offen lds
	s_mov_b32 m0, s40
	s_nop 0
	buffer_load_dwordx4 v74, s[4:7], s43 offen lds
	s_mov_b32 m0, s41
	s_waitcnt lgkmcnt(2)
	v_mfma_f32_32x32x16_f16 v[50:65], v[120:123], v[124:127], v[50:65]
	buffer_load_dwordx4 v73, s[12:15], s43 offen lds
	s_mov_b32 m0, s42
	s_nop 0
	buffer_load_dwordx4 v75, s[12:15], s43 offen lds
	s_waitcnt vmcnt(8)
	s_barrier
	s_add_i32 s43, s0, 0x800
	s_waitcnt lgkmcnt(1)
	v_mfma_f32_32x32x16_f16 v[18:33], v[120:123], v[128:131], v[18:33]
	s_mov_b32 m0, s1
	s_waitcnt lgkmcnt(0)
	v_mfma_f32_32x32x16_f16 v[34:49], v[132:135], v[124:127], v[34:49]
	v_mfma_f32_32x32x16_f16 v[2:17], v[132:135], v[128:131], v[2:17]
	ds_read_b128 v[120:123], v110 offset:16384
	ds_read_b128 v[124:127], v111
	ds_read_b128 v[128:131], v111 offset:4096
	ds_read_b128 v[132:135], v110 offset:20480
	s_waitcnt lgkmcnt(2)
	v_mfma_f32_32x32x16_f16 v[50:65], v[120:123], v[124:127], v[50:65]
	s_waitcnt lgkmcnt(1)
	v_mfma_f32_32x32x16_f16 v[18:33], v[120:123], v[128:131], v[18:33]
	s_waitcnt lgkmcnt(0)
	v_mfma_f32_32x32x16_f16 v[34:49], v[132:135], v[124:127], v[34:49]
	v_mfma_f32_32x32x16_f16 v[2:17], v[132:135], v[128:131], v[2:17]
	ds_read_b128 v[120:123], v67 offset:16384
	ds_read_b128 v[124:127], v109
	ds_read_b128 v[128:131], v109 offset:4096
	ds_read_b128 v[132:135], v67 offset:20480
	buffer_load_dwordx4 v72, s[4:7], s43 offen lds
	s_mov_b32 m0, s2
	s_nop 0
	buffer_load_dwordx4 v74, s[4:7], s43 offen lds
	s_mov_b32 m0, s3
	s_waitcnt lgkmcnt(2)
	v_mfma_f32_32x32x16_f16 v[50:65], v[120:123], v[124:127], v[50:65]
	buffer_load_dwordx4 v73, s[12:15], s43 offen lds
	s_mov_b32 m0, s18
	s_nop 0
	buffer_load_dwordx4 v75, s[12:15], s43 offen lds
	s_waitcnt vmcnt(8)
	s_barrier
	s_add_i32 s43, s0, 0x880
	s_waitcnt lgkmcnt(1)
	v_mfma_f32_32x32x16_f16 v[18:33], v[120:123], v[128:131], v[18:33]
	s_mov_b32 m0, s19
	s_waitcnt lgkmcnt(0)
	v_mfma_f32_32x32x16_f16 v[34:49], v[132:135], v[124:127], v[34:49]
	v_mfma_f32_32x32x16_f16 v[2:17], v[132:135], v[128:131], v[2:17]
	ds_read_b128 v[120:123], v110 offset:49152
	ds_read_b128 v[124:127], v111 offset:32768
	ds_read_b128 v[128:131], v111 offset:36864
	ds_read_b128 v[132:135], v110 offset:53248
	s_waitcnt lgkmcnt(2)
	v_mfma_f32_32x32x16_f16 v[50:65], v[120:123], v[124:127], v[50:65]
	s_waitcnt lgkmcnt(1)
	v_mfma_f32_32x32x16_f16 v[18:33], v[120:123], v[128:131], v[18:33]
	s_waitcnt lgkmcnt(0)
	v_mfma_f32_32x32x16_f16 v[34:49], v[132:135], v[124:127], v[34:49]
	v_mfma_f32_32x32x16_f16 v[2:17], v[132:135], v[128:131], v[2:17]
	ds_read_b128 v[120:123], v67 offset:49152
	ds_read_b128 v[124:127], v109 offset:32768
	ds_read_b128 v[128:131], v109 offset:36864
	ds_read_b128 v[132:135], v67 offset:53248
	buffer_load_dwordx4 v72, s[4:7], s43 offen lds
	s_mov_b32 m0, s31
	s_nop 0
	buffer_load_dwordx4 v74, s[4:7], s43 offen lds
	s_mov_b32 m0, s33
	s_waitcnt lgkmcnt(2)
	v_mfma_f32_32x32x16_f16 v[50:65], v[120:123], v[124:127], v[50:65]
	buffer_load_dwordx4 v73, s[12:15], s43 offen lds
	s_mov_b32 m0, s34
	s_nop 0
	buffer_load_dwordx4 v75, s[12:15], s43 offen lds
	s_waitcnt vmcnt(8)
	s_barrier
	s_add_i32 s43, s0, 0x900
	s_waitcnt lgkmcnt(1)
	v_mfma_f32_32x32x16_f16 v[18:33], v[120:123], v[128:131], v[18:33]
	s_mov_b32 m0, s35
	s_waitcnt lgkmcnt(0)
	v_mfma_f32_32x32x16_f16 v[34:49], v[132:135], v[124:127], v[34:49]
	v_mfma_f32_32x32x16_f16 v[2:17], v[132:135], v[128:131], v[2:17]
	ds_read_b128 v[120:123], v96
	ds_read_b128 v[124:127], v113
	ds_read_b128 v[128:131], v113 offset:4096
	ds_read_b128 v[132:135], v112 offset:4096
	s_waitcnt lgkmcnt(2)
	v_mfma_f32_32x32x16_f16 v[50:65], v[120:123], v[124:127], v[50:65]
	s_waitcnt lgkmcnt(1)
	v_mfma_f32_32x32x16_f16 v[18:33], v[120:123], v[128:131], v[18:33]
	s_waitcnt lgkmcnt(0)
	v_mfma_f32_32x32x16_f16 v[34:49], v[132:135], v[124:127], v[34:49]
	v_mfma_f32_32x32x16_f16 v[2:17], v[132:135], v[128:131], v[2:17]
	ds_read_b128 v[120:123], v97
	ds_read_b128 v[124:127], v115
	ds_read_b128 v[128:131], v115 offset:4096
	ds_read_b128 v[132:135], v114 offset:4096
	buffer_load_dwordx4 v72, s[4:7], s43 offen lds
	s_mov_b32 m0, s36
	s_nop 0
	buffer_load_dwordx4 v74, s[4:7], s43 offen lds
	s_mov_b32 m0, s37
	s_waitcnt lgkmcnt(2)
	v_mfma_f32_32x32x16_f16 v[50:65], v[120:123], v[124:127], v[50:65]
	buffer_load_dwordx4 v73, s[12:15], s43 offen lds
	s_mov_b32 m0, s38
	s_nop 0
	buffer_load_dwordx4 v75, s[12:15], s43 offen lds
	s_waitcnt vmcnt(8)
	s_barrier
	s_add_i32 s43, s0, 0x980
	s_waitcnt lgkmcnt(1)
	v_mfma_f32_32x32x16_f16 v[18:33], v[120:123], v[128:131], v[18:33]
	s_mov_b32 m0, s39
	s_waitcnt lgkmcnt(0)
	v_mfma_f32_32x32x16_f16 v[34:49], v[132:135], v[124:127], v[34:49]
	v_mfma_f32_32x32x16_f16 v[2:17], v[132:135], v[128:131], v[2:17]
	ds_read_b128 v[120:123], v98
	ds_read_b128 v[124:127], v117
	ds_read_b128 v[128:131], v117 offset:4096
	ds_read_b128 v[132:135], v116 offset:4096
	s_waitcnt lgkmcnt(2)
	v_mfma_f32_32x32x16_f16 v[50:65], v[120:123], v[124:127], v[50:65]
	s_waitcnt lgkmcnt(1)
	v_mfma_f32_32x32x16_f16 v[18:33], v[120:123], v[128:131], v[18:33]
	s_waitcnt lgkmcnt(0)
	v_mfma_f32_32x32x16_f16 v[34:49], v[132:135], v[124:127], v[34:49]
	v_mfma_f32_32x32x16_f16 v[2:17], v[132:135], v[128:131], v[2:17]
	ds_read_b128 v[120:123], v99
	ds_read_b128 v[124:127], v119
	ds_read_b128 v[128:131], v119 offset:4096
	ds_read_b128 v[132:135], v118 offset:4096
	buffer_load_dwordx4 v72, s[4:7], s43 offen lds
	s_mov_b32 m0, s40
	s_nop 0
	buffer_load_dwordx4 v74, s[4:7], s43 offen lds
	s_mov_b32 m0, s41
	s_waitcnt lgkmcnt(2)
	v_mfma_f32_32x32x16_f16 v[50:65], v[120:123], v[124:127], v[50:65]
	buffer_load_dwordx4 v73, s[12:15], s43 offen lds
	s_mov_b32 m0, s42
	s_nop 0
	buffer_load_dwordx4 v75, s[12:15], s43 offen lds
	s_waitcnt vmcnt(8)
	s_barrier
	s_add_i32 s43, s0, 0xa00
	s_waitcnt lgkmcnt(1)
	v_mfma_f32_32x32x16_f16 v[18:33], v[120:123], v[128:131], v[18:33]
	s_mov_b32 m0, s1
	s_waitcnt lgkmcnt(0)
	v_mfma_f32_32x32x16_f16 v[34:49], v[132:135], v[124:127], v[34:49]
	v_mfma_f32_32x32x16_f16 v[2:17], v[132:135], v[128:131], v[2:17]
	ds_read_b128 v[120:123], v110 offset:16384
	ds_read_b128 v[124:127], v111
	ds_read_b128 v[128:131], v111 offset:4096
	ds_read_b128 v[132:135], v110 offset:20480
	s_waitcnt lgkmcnt(2)
	v_mfma_f32_32x32x16_f16 v[50:65], v[120:123], v[124:127], v[50:65]
	s_waitcnt lgkmcnt(1)
	v_mfma_f32_32x32x16_f16 v[18:33], v[120:123], v[128:131], v[18:33]
	s_waitcnt lgkmcnt(0)
	v_mfma_f32_32x32x16_f16 v[34:49], v[132:135], v[124:127], v[34:49]
	v_mfma_f32_32x32x16_f16 v[2:17], v[132:135], v[128:131], v[2:17]
	ds_read_b128 v[120:123], v67 offset:16384
	ds_read_b128 v[124:127], v109
	ds_read_b128 v[128:131], v109 offset:4096
	ds_read_b128 v[132:135], v67 offset:20480
	buffer_load_dwordx4 v72, s[4:7], s43 offen lds
	s_mov_b32 m0, s2
	s_nop 0
	buffer_load_dwordx4 v74, s[4:7], s43 offen lds
	s_mov_b32 m0, s3
	s_waitcnt lgkmcnt(2)
	v_mfma_f32_32x32x16_f16 v[50:65], v[120:123], v[124:127], v[50:65]
	buffer_load_dwordx4 v73, s[12:15], s43 offen lds
	s_mov_b32 m0, s18
	s_nop 0
	buffer_load_dwordx4 v75, s[12:15], s43 offen lds
	s_waitcnt vmcnt(8)
	s_barrier
	s_add_i32 s43, s0, 0xa80
	s_waitcnt lgkmcnt(1)
	v_mfma_f32_32x32x16_f16 v[18:33], v[120:123], v[128:131], v[18:33]
	s_mov_b32 m0, s19
	s_waitcnt lgkmcnt(0)
	v_mfma_f32_32x32x16_f16 v[34:49], v[132:135], v[124:127], v[34:49]
	v_mfma_f32_32x32x16_f16 v[2:17], v[132:135], v[128:131], v[2:17]
	ds_read_b128 v[120:123], v110 offset:49152
	ds_read_b128 v[124:127], v111 offset:32768
	ds_read_b128 v[128:131], v111 offset:36864
	ds_read_b128 v[132:135], v110 offset:53248
	s_waitcnt lgkmcnt(2)
	v_mfma_f32_32x32x16_f16 v[50:65], v[120:123], v[124:127], v[50:65]
	s_waitcnt lgkmcnt(1)
	v_mfma_f32_32x32x16_f16 v[18:33], v[120:123], v[128:131], v[18:33]
	s_waitcnt lgkmcnt(0)
	v_mfma_f32_32x32x16_f16 v[34:49], v[132:135], v[124:127], v[34:49]
	v_mfma_f32_32x32x16_f16 v[2:17], v[132:135], v[128:131], v[2:17]
	ds_read_b128 v[120:123], v67 offset:49152
	ds_read_b128 v[124:127], v109 offset:32768
	ds_read_b128 v[128:131], v109 offset:36864
	ds_read_b128 v[132:135], v67 offset:53248
	buffer_load_dwordx4 v72, s[4:7], s43 offen lds
	s_mov_b32 m0, s31
	s_nop 0
	buffer_load_dwordx4 v74, s[4:7], s43 offen lds
	s_mov_b32 m0, s33
	s_waitcnt lgkmcnt(2)
	v_mfma_f32_32x32x16_f16 v[50:65], v[120:123], v[124:127], v[50:65]
	buffer_load_dwordx4 v73, s[12:15], s43 offen lds
	s_mov_b32 m0, s34
	s_nop 0
	buffer_load_dwordx4 v75, s[12:15], s43 offen lds
	s_waitcnt vmcnt(8)
	s_barrier
	s_add_i32 s43, s0, 0xb00
	s_waitcnt lgkmcnt(1)
	v_mfma_f32_32x32x16_f16 v[18:33], v[120:123], v[128:131], v[18:33]
	s_mov_b32 m0, s35
	s_waitcnt lgkmcnt(0)
	v_mfma_f32_32x32x16_f16 v[34:49], v[132:135], v[124:127], v[34:49]
	v_mfma_f32_32x32x16_f16 v[2:17], v[132:135], v[128:131], v[2:17]
	ds_read_b128 v[120:123], v96
	ds_read_b128 v[124:127], v113
	ds_read_b128 v[128:131], v113 offset:4096
	ds_read_b128 v[132:135], v112 offset:4096
	s_waitcnt lgkmcnt(2)
	v_mfma_f32_32x32x16_f16 v[50:65], v[120:123], v[124:127], v[50:65]
	s_waitcnt lgkmcnt(1)
	v_mfma_f32_32x32x16_f16 v[18:33], v[120:123], v[128:131], v[18:33]
	s_waitcnt lgkmcnt(0)
	v_mfma_f32_32x32x16_f16 v[34:49], v[132:135], v[124:127], v[34:49]
	v_mfma_f32_32x32x16_f16 v[2:17], v[132:135], v[128:131], v[2:17]
	ds_read_b128 v[120:123], v97
	ds_read_b128 v[124:127], v115
	ds_read_b128 v[128:131], v115 offset:4096
	ds_read_b128 v[132:135], v114 offset:4096
	buffer_load_dwordx4 v72, s[4:7], s43 offen lds
	s_mov_b32 m0, s36
	s_nop 0
	buffer_load_dwordx4 v74, s[4:7], s43 offen lds
	s_mov_b32 m0, s37
	s_waitcnt lgkmcnt(2)
	v_mfma_f32_32x32x16_f16 v[50:65], v[120:123], v[124:127], v[50:65]
	buffer_load_dwordx4 v73, s[12:15], s43 offen lds
	s_mov_b32 m0, s38
	s_nop 0
	buffer_load_dwordx4 v75, s[12:15], s43 offen lds
	s_waitcnt vmcnt(8)
	s_barrier
	s_add_i32 s43, s0, 0xb80
	s_waitcnt lgkmcnt(1)
	v_mfma_f32_32x32x16_f16 v[18:33], v[120:123], v[128:131], v[18:33]
	s_mov_b32 m0, s39
	s_waitcnt lgkmcnt(0)
	v_mfma_f32_32x32x16_f16 v[34:49], v[132:135], v[124:127], v[34:49]
	v_mfma_f32_32x32x16_f16 v[2:17], v[132:135], v[128:131], v[2:17]
	ds_read_b128 v[120:123], v98
	ds_read_b128 v[124:127], v117
	ds_read_b128 v[128:131], v117 offset:4096
	ds_read_b128 v[132:135], v116 offset:4096
	s_waitcnt lgkmcnt(2)
	v_mfma_f32_32x32x16_f16 v[50:65], v[120:123], v[124:127], v[50:65]
	s_waitcnt lgkmcnt(1)
	v_mfma_f32_32x32x16_f16 v[18:33], v[120:123], v[128:131], v[18:33]
	s_waitcnt lgkmcnt(0)
	v_mfma_f32_32x32x16_f16 v[34:49], v[132:135], v[124:127], v[34:49]
	v_mfma_f32_32x32x16_f16 v[2:17], v[132:135], v[128:131], v[2:17]
	ds_read_b128 v[120:123], v99
	ds_read_b128 v[124:127], v119
	ds_read_b128 v[128:131], v119 offset:4096
	ds_read_b128 v[132:135], v118 offset:4096
	buffer_load_dwordx4 v72, s[4:7], s43 offen lds
	s_mov_b32 m0, s40
	s_nop 0
	buffer_load_dwordx4 v74, s[4:7], s43 offen lds
	s_mov_b32 m0, s41
	s_waitcnt lgkmcnt(2)
	v_mfma_f32_32x32x16_f16 v[50:65], v[120:123], v[124:127], v[50:65]
	buffer_load_dwordx4 v73, s[12:15], s43 offen lds
	s_mov_b32 m0, s42
	s_nop 0
	buffer_load_dwordx4 v75, s[12:15], s43 offen lds
	s_waitcnt vmcnt(8)
	s_barrier
	s_add_i32 s43, s0, 0xc00
	s_waitcnt lgkmcnt(1)
	v_mfma_f32_32x32x16_f16 v[18:33], v[120:123], v[128:131], v[18:33]
	s_mov_b32 m0, s1
	s_waitcnt lgkmcnt(0)
	v_mfma_f32_32x32x16_f16 v[34:49], v[132:135], v[124:127], v[34:49]
	v_mfma_f32_32x32x16_f16 v[2:17], v[132:135], v[128:131], v[2:17]
	ds_read_b128 v[120:123], v110 offset:16384
	ds_read_b128 v[124:127], v111
	ds_read_b128 v[128:131], v111 offset:4096
	ds_read_b128 v[132:135], v110 offset:20480
	s_waitcnt lgkmcnt(2)
	v_mfma_f32_32x32x16_f16 v[50:65], v[120:123], v[124:127], v[50:65]
	s_waitcnt lgkmcnt(1)
	v_mfma_f32_32x32x16_f16 v[18:33], v[120:123], v[128:131], v[18:33]
	s_waitcnt lgkmcnt(0)
	v_mfma_f32_32x32x16_f16 v[34:49], v[132:135], v[124:127], v[34:49]
	v_mfma_f32_32x32x16_f16 v[2:17], v[132:135], v[128:131], v[2:17]
	ds_read_b128 v[120:123], v67 offset:16384
	ds_read_b128 v[124:127], v109
	ds_read_b128 v[128:131], v109 offset:4096
	ds_read_b128 v[132:135], v67 offset:20480
	buffer_load_dwordx4 v72, s[4:7], s43 offen lds
	s_mov_b32 m0, s2
	s_nop 0
	buffer_load_dwordx4 v74, s[4:7], s43 offen lds
	s_mov_b32 m0, s3
	s_waitcnt lgkmcnt(2)
	v_mfma_f32_32x32x16_f16 v[50:65], v[120:123], v[124:127], v[50:65]
	buffer_load_dwordx4 v73, s[12:15], s43 offen lds
	s_mov_b32 m0, s18
	s_nop 0
	buffer_load_dwordx4 v75, s[12:15], s43 offen lds
	s_waitcnt vmcnt(8)
	s_barrier
	s_add_i32 s43, s0, 0xc80
	s_waitcnt lgkmcnt(1)
	v_mfma_f32_32x32x16_f16 v[18:33], v[120:123], v[128:131], v[18:33]
	s_mov_b32 m0, s19
	s_add_i32 s19, s0, 0xd00
	s_waitcnt lgkmcnt(0)
	v_mfma_f32_32x32x16_f16 v[34:49], v[132:135], v[124:127], v[34:49]
	v_mfma_f32_32x32x16_f16 v[2:17], v[132:135], v[128:131], v[2:17]
	ds_read_b128 v[120:123], v110 offset:49152
	ds_read_b128 v[124:127], v111 offset:32768
	ds_read_b128 v[128:131], v111 offset:36864
	ds_read_b128 v[132:135], v110 offset:53248
	s_waitcnt lgkmcnt(2)
	v_mfma_f32_32x32x16_f16 v[50:65], v[120:123], v[124:127], v[50:65]
	s_waitcnt lgkmcnt(1)
	v_mfma_f32_32x32x16_f16 v[18:33], v[120:123], v[128:131], v[18:33]
	s_waitcnt lgkmcnt(0)
	v_mfma_f32_32x32x16_f16 v[34:49], v[132:135], v[124:127], v[34:49]
	v_mfma_f32_32x32x16_f16 v[2:17], v[132:135], v[128:131], v[2:17]
	ds_read_b128 v[120:123], v67 offset:49152
	ds_read_b128 v[124:127], v109 offset:32768
	ds_read_b128 v[128:131], v109 offset:36864
	ds_read_b128 v[132:135], v67 offset:53248
	buffer_load_dwordx4 v72, s[4:7], s43 offen lds
	s_mov_b32 m0, s31
	s_add_i32 s31, s0, 0xe00
	buffer_load_dwordx4 v74, s[4:7], s43 offen lds
	s_mov_b32 m0, s33
	s_waitcnt lgkmcnt(2)
	v_mfma_f32_32x32x16_f16 v[50:65], v[120:123], v[124:127], v[50:65]
	buffer_load_dwordx4 v73, s[12:15], s43 offen lds
	s_mov_b32 m0, s34
	s_nop 0
	buffer_load_dwordx4 v75, s[12:15], s43 offen lds
	s_waitcnt vmcnt(8)
	s_barrier
	s_mov_b32 m0, s35
	s_waitcnt lgkmcnt(1)
	v_mfma_f32_32x32x16_f16 v[18:33], v[120:123], v[128:131], v[18:33]
	s_waitcnt lgkmcnt(0)
	v_mfma_f32_32x32x16_f16 v[34:49], v[132:135], v[124:127], v[34:49]
	v_mfma_f32_32x32x16_f16 v[2:17], v[132:135], v[128:131], v[2:17]
	ds_read_b128 v[120:123], v96
	ds_read_b128 v[124:127], v113
	ds_read_b128 v[128:131], v113 offset:4096
	ds_read_b128 v[132:135], v112 offset:4096
	s_waitcnt lgkmcnt(2)
	v_mfma_f32_32x32x16_f16 v[50:65], v[120:123], v[124:127], v[50:65]
	s_waitcnt lgkmcnt(1)
	v_mfma_f32_32x32x16_f16 v[18:33], v[120:123], v[128:131], v[18:33]
	s_waitcnt lgkmcnt(0)
	v_mfma_f32_32x32x16_f16 v[34:49], v[132:135], v[124:127], v[34:49]
	v_mfma_f32_32x32x16_f16 v[2:17], v[132:135], v[128:131], v[2:17]
	ds_read_b128 v[120:123], v97
	ds_read_b128 v[124:127], v115
	ds_read_b128 v[128:131], v115 offset:4096
	ds_read_b128 v[132:135], v114 offset:4096
	buffer_load_dwordx4 v72, s[4:7], s19 offen lds
	s_mov_b32 m0, s36
	s_nop 0
	buffer_load_dwordx4 v74, s[4:7], s19 offen lds
	s_mov_b32 m0, s37
	s_waitcnt lgkmcnt(2)
	v_mfma_f32_32x32x16_f16 v[50:65], v[120:123], v[124:127], v[50:65]
	buffer_load_dwordx4 v73, s[12:15], s19 offen lds
	s_mov_b32 m0, s38
	s_nop 0
	buffer_load_dwordx4 v75, s[12:15], s19 offen lds
	s_waitcnt vmcnt(8)
	s_barrier
	s_add_i32 s19, s0, 0xd80
	s_waitcnt lgkmcnt(1)
	v_mfma_f32_32x32x16_f16 v[18:33], v[120:123], v[128:131], v[18:33]
	s_mov_b32 m0, s39
	s_ashr_i32 s0, s23, 31
	s_xor_b32 s0, s0, s25
	s_waitcnt lgkmcnt(0)
	v_mfma_f32_32x32x16_f16 v[34:49], v[132:135], v[124:127], v[34:49]
	v_mfma_f32_32x32x16_f16 v[2:17], v[132:135], v[128:131], v[2:17]
	ds_read_b128 v[120:123], v98
	ds_read_b128 v[124:127], v117
	ds_read_b128 v[128:131], v117 offset:4096
	ds_read_b128 v[132:135], v116 offset:4096
	s_waitcnt lgkmcnt(2)
	v_mfma_f32_32x32x16_f16 v[50:65], v[120:123], v[124:127], v[50:65]
	s_waitcnt lgkmcnt(1)
	v_mfma_f32_32x32x16_f16 v[18:33], v[120:123], v[128:131], v[18:33]
	s_waitcnt lgkmcnt(0)
	v_mfma_f32_32x32x16_f16 v[34:49], v[132:135], v[124:127], v[34:49]
	v_mfma_f32_32x32x16_f16 v[2:17], v[132:135], v[128:131], v[2:17]
	ds_read_b128 v[120:123], v99
	ds_read_b128 v[124:127], v119
	ds_read_b128 v[128:131], v119 offset:4096
	ds_read_b128 v[132:135], v118 offset:4096
	buffer_load_dwordx4 v72, s[4:7], s19 offen lds
	s_mov_b32 m0, s40
	s_nop 0
	buffer_load_dwordx4 v74, s[4:7], s19 offen lds
	s_mov_b32 m0, s41
	s_waitcnt lgkmcnt(2)
	v_mfma_f32_32x32x16_f16 v[50:65], v[120:123], v[124:127], v[50:65]
	buffer_load_dwordx4 v73, s[12:15], s19 offen lds
	s_mov_b32 m0, s42
	s_nop 0
	buffer_load_dwordx4 v75, s[12:15], s19 offen lds
	s_waitcnt vmcnt(8)
	s_barrier
	s_mov_b32 m0, s1
	s_waitcnt lgkmcnt(1)
	v_mfma_f32_32x32x16_f16 v[18:33], v[120:123], v[128:131], v[18:33]
	s_abs_i32 s1, s23
	s_waitcnt lgkmcnt(0)
	v_mfma_f32_32x32x16_f16 v[34:49], v[132:135], v[124:127], v[34:49]
	v_mfma_f32_32x32x16_f16 v[2:17], v[132:135], v[128:131], v[2:17]
	ds_read_b128 v[120:123], v110 offset:16384
	ds_read_b128 v[124:127], v111
	ds_read_b128 v[128:131], v111 offset:4096
	ds_read_b128 v[132:135], v110 offset:20480
	s_waitcnt lgkmcnt(2)
	v_mfma_f32_32x32x16_f16 v[50:65], v[120:123], v[124:127], v[50:65]
	s_waitcnt lgkmcnt(1)
	v_mfma_f32_32x32x16_f16 v[18:33], v[120:123], v[128:131], v[18:33]
	s_waitcnt lgkmcnt(0)
	v_mfma_f32_32x32x16_f16 v[34:49], v[132:135], v[124:127], v[34:49]
	v_mfma_f32_32x32x16_f16 v[2:17], v[132:135], v[128:131], v[2:17]
	ds_read_b128 v[120:123], v67 offset:16384
	ds_read_b128 v[124:127], v109
	ds_read_b128 v[128:131], v109 offset:4096
	ds_read_b128 v[132:135], v67 offset:20480
	buffer_load_dwordx4 v72, s[4:7], s31 offen lds
	s_mov_b32 m0, s2
	s_mul_hi_u32 s2, s1, s26
	buffer_load_dwordx4 v74, s[4:7], s31 offen lds
	s_mov_b32 m0, s3
	s_mul_i32 s3, s2, s24
	s_waitcnt lgkmcnt(2)
	v_mfma_f32_32x32x16_f16 v[50:65], v[120:123], v[124:127], v[50:65]
	buffer_load_dwordx4 v73, s[12:15], s31 offen lds
	s_mov_b32 m0, s18
	s_sub_i32 s1, s1, s3
	buffer_load_dwordx4 v75, s[12:15], s31 offen lds
	s_waitcnt vmcnt(8)
	s_barrier
	s_add_i32 s3, s2, 1
	s_waitcnt lgkmcnt(1)
	v_mfma_f32_32x32x16_f16 v[18:33], v[120:123], v[128:131], v[18:33]
	s_sub_i32 s14, s1, s24
	s_cmp_ge_u32 s1, s24
	s_cselect_b32 s2, s3, s2
	s_cselect_b32 s1, s14, s1
	s_add_i32 s3, s2, 1
	s_cmp_ge_u32 s1, s24
	s_cselect_b32 s1, s3, s2
	s_waitcnt lgkmcnt(0)
	v_mfma_f32_32x32x16_f16 v[34:49], v[132:135], v[124:127], v[34:49]
	s_xor_b32 s1, s1, s0
	s_sub_i32 s0, s1, s0
	s_mul_i32 s1, s0, s21
	s_sub_i32 s15, s23, s1
	s_lshl_b32 s2, s15, 7
	s_lshl_b32 s14, s0, 7
	s_ashr_i32 s3, s2, 31
	v_mfma_f32_32x32x16_f16 v[2:17], v[132:135], v[128:131], v[2:17]
	ds_read_b128 v[120:123], v110 offset:49152
	ds_read_b128 v[124:127], v111 offset:32768
	ds_read_b128 v[128:131], v111 offset:36864
	ds_read_b128 v[132:135], v110 offset:53248
	s_waitcnt lgkmcnt(2)
	v_mfma_f32_32x32x16_f16 v[50:65], v[120:123], v[124:127], v[50:65]
	s_waitcnt lgkmcnt(1)
	v_mfma_f32_32x32x16_f16 v[18:33], v[120:123], v[128:131], v[18:33]
	s_waitcnt lgkmcnt(0)
	v_mfma_f32_32x32x16_f16 v[34:49], v[132:135], v[124:127], v[34:49]
	v_mfma_f32_32x32x16_f16 v[2:17], v[132:135], v[128:131], v[2:17]
	ds_read_b128 v[120:123], v67 offset:49152
	ds_read_b128 v[124:127], v109 offset:32768
	ds_read_b128 v[128:131], v109 offset:36864
	ds_read_b128 v[132:135], v67 offset:53248
	s_waitcnt vmcnt(4)
	s_barrier
	s_waitcnt lgkmcnt(2)
	v_mfma_f32_32x32x16_f16 v[50:65], v[120:123], v[124:127], v[50:65]
	s_waitcnt lgkmcnt(1)
	v_mfma_f32_32x32x16_f16 v[18:33], v[120:123], v[128:131], v[18:33]
	s_waitcnt lgkmcnt(0)
	v_mfma_f32_32x32x16_f16 v[34:49], v[132:135], v[124:127], v[34:49]
	v_mfma_f32_32x32x16_f16 v[2:17], v[132:135], v[128:131], v[2:17]
	ds_read_b128 v[120:123], v96
	ds_read_b128 v[124:127], v113
	ds_read_b128 v[128:131], v113 offset:4096
	ds_read_b128 v[110:113], v112 offset:4096
	s_waitcnt lgkmcnt(2)
	v_mfma_f32_32x32x16_f16 v[50:65], v[120:123], v[124:127], v[50:65]
	s_waitcnt lgkmcnt(1)
	v_mfma_f32_32x32x16_f16 v[18:33], v[120:123], v[128:131], v[18:33]
	s_waitcnt lgkmcnt(0)
	v_mfma_f32_32x32x16_f16 v[34:49], v[110:113], v[124:127], v[34:49]
	ds_read_b128 v[120:123], v97
	ds_read_b128 v[124:127], v115
	ds_read_b128 v[132:135], v115 offset:4096
	s_waitcnt lgkmcnt(1)
	v_mfma_f32_32x32x16_f16 v[50:65], v[120:123], v[124:127], v[50:65]
	s_waitcnt lgkmcnt(0)
	v_mfma_f32_32x32x16_f16 v[18:33], v[120:123], v[132:135], v[18:33]
	ds_read_b128 v[120:123], v114 offset:4096
	s_waitcnt vmcnt(0)
	s_barrier
	v_mfma_f32_32x32x16_f16 v[2:17], v[110:113], v[128:131], v[2:17]
	s_waitcnt lgkmcnt(0)
	v_mfma_f32_32x32x16_f16 v[34:49], v[120:123], v[124:127], v[34:49]
	ds_read_b128 v[124:127], v98
	ds_read_b128 v[136:139], v117
	ds_read_b128 v[140:143], v117 offset:4096
	ds_read_b128 v[114:117], v116 offset:4096
	s_waitcnt lgkmcnt(2)
	v_mfma_f32_32x32x16_f16 v[50:65], v[124:127], v[136:139], v[50:65]
	s_waitcnt lgkmcnt(1)
	v_mfma_f32_32x32x16_f16 v[18:33], v[124:127], v[140:143], v[18:33]
	v_mfma_f32_32x32x16_f16 v[2:17], v[120:123], v[132:135], v[2:17]
	s_waitcnt lgkmcnt(0)
	v_mfma_f32_32x32x16_f16 v[34:49], v[114:117], v[136:139], v[34:49]
	ds_read_b128 v[124:127], v99
	ds_read_b128 v[136:139], v119
	ds_read_b128 v[144:147], v119 offset:4096
	s_waitcnt lgkmcnt(1)
	v_mfma_f32_32x32x16_f16 v[50:65], v[124:127], v[136:139], v[50:65]
	s_waitcnt lgkmcnt(0)
	v_mfma_f32_32x32x16_f16 v[18:33], v[124:127], v[144:147], v[18:33]
	ds_read_b128 v[124:127], v118 offset:4096
	s_waitcnt lgkmcnt(0)
	s_barrier
	s_nop 8
	ds_write_b128 v100, v[50:53]
	ds_write_b128 v101, v[54:57]
	v_mfma_f32_32x32x16_f16 v[2:17], v[114:117], v[140:143], v[2:17]
	s_waitcnt lgkmcnt(2)
	v_mfma_f32_32x32x16_f16 v[2:17], v[124:127], v[144:147], v[2:17]
	v_mfma_f32_32x32x16_f16 v[34:49], v[124:127], v[136:139], v[34:49]
	ds_write_b128 v102, v[58:61]
	ds_write_b128 v103, v[62:65]
	s_nop 9
	ds_write_b128 v104, v[34:37]
	ds_write_b128 v105, v[38:41]
	ds_write_b128 v106, v[42:45]
	ds_write_b128 v107, v[46:49]
	ds_write_b128 v100, v[18:21] offset:16384
	ds_write_b128 v101, v[22:25] offset:16384
	ds_write_b128 v102, v[26:29] offset:16384
	ds_write_b128 v103, v[30:33] offset:16384
	ds_write_b128 v104, v[2:5] offset:16384
	ds_write_b128 v105, v[6:9] offset:16384
	ds_write_b128 v106, v[10:13] offset:16384
	ds_write_b128 v107, v[14:17] offset:16384
	v_or_b32_e32 v25, s14, v1
	v_lshl_add_u64 v[22:23], s[2:3], 1, v[70:71]
	s_waitcnt lgkmcnt(0)
	s_barrier
	v_mad_i64_i32 v[2:3], s[0:1], v25, s29, v[22:23]
	v_mov_b64_e32 v[10:11], v[160:161]
	v_mov_b64_e32 v[12:13], v[162:163]
	v_lshl_add_u64 v[14:15], s[2:3], 2, v[68:69]
	v_mov_b64_e32 v[6:7], v[176:177]
	v_mov_b64_e32 v[8:9], v[178:179]
	v_mov_b64_e32 v[2:3], v[180:181]
	v_mov_b64_e32 v[4:5], v[182:183]
	v_add_u32_e32 v14, 0, v85
	v_add_u32_e32 v18, s28, v85
	ds_read_b128 v[14:17], v14
	ds_read_b128 v[26:29], v18
	v_or_b32_e32 v18, 32, v25
	v_mad_i64_i32 v[18:19], s[0:1], v18, s29, v[22:23]
	v_mov_b64_e32 v[18:19], v[164:165]
	v_mov_b64_e32 v[20:21], v[166:167]
	s_waitcnt lgkmcnt(0)
	v_pk_add_f32 v[16:17], v[16:17], v[28:29]
	v_add_f32_e32 v35, v14, v26
	v_mov_b32_e32 v34, v27
	v_xor_b32_e32 v24, 8, v108
	v_cvt_f32_f16_e32 v30, v11
	v_cvt_f32_f16_sdwa v31, v11 dst_sel:DWORD dst_unused:UNUSED_PAD src0_sel:WORD_1
	v_add_u32_e32 v11, 0, v86
	v_pk_add_f32 v[16:17], v[8:9], v[16:17]
	ds_read_b128 v[26:29], v11
	v_add_u32_e32 v11, s28, v86
	v_pk_add_f32 v[36:37], v[16:17], v[30:31]
	ds_read_b128 v[30:33], v11
	v_cvt_f32_f16_e32 v38, v13
	v_cvt_f32_f16_sdwa v39, v13 dst_sel:DWORD dst_unused:UNUSED_PAD src0_sel:WORD_1
	v_mov_b32_e32 v16, v2
	v_mov_b32_e32 v17, v3
	s_waitcnt lgkmcnt(0)
	v_pk_add_f32 v[28:29], v[28:29], v[32:33]
	v_cvt_f32_f16_e32 v32, v10
	v_pk_add_f32 v[28:29], v[4:5], v[28:29]
	v_pk_mov_b32 v[16:17], v[26:27], v[16:17] op_sel:[1,0]
	v_pk_add_f32 v[28:29], v[28:29], v[38:39]
	v_cvt_f32_f16_e32 v38, v12
	v_add_f32_e32 v26, v26, v30
	v_cvt_f32_f16_sdwa v33, v10 dst_sel:DWORD dst_unused:UNUSED_PAD src0_sel:WORD_1
	v_cvt_f32_f16_sdwa v30, v12 dst_sel:DWORD dst_unused:UNUSED_PAD src0_sel:WORD_1
	v_or_b32_e32 v12, 64, v25
	v_pk_mov_b32 v[14:15], v[14:15], v[6:7] op_sel:[1,0]
	v_mad_i64_i32 v[40:41], s[0:1], v12, s29, v[22:23]
	v_or_b32_e32 v12, 0x60, v25
	v_mov_b32_e32 v10, v31
	v_mov_b32_e32 v11, v26
	v_mad_i64_i32 v[42:43], s[0:1], v12, s29, v[22:23]
	v_pk_add_f32 v[44:45], v[14:15], v[34:35]
	v_mov_b32_e32 v12, v7
	v_mov_b32_e32 v13, v32
	v_pk_add_f32 v[10:11], v[16:17], v[10:11]
	v_pk_add_f32 v[46:47], v[12:13], v[44:45]
	v_mov_b32_e32 v22, v3
	v_mov_b32_e32 v23, v38
	v_pk_add_f32 v[48:49], v[22:23], v[10:11]
	v_mov_b32_e32 v10, v33
	v_mov_b32_e32 v11, v47
	v_pk_add_f32 v[50:51], v[46:47], v[10:11]
	v_mov_b64_e32 v[14:15], v[168:169]
	v_mov_b64_e32 v[16:17], v[170:171]
	v_mov_b64_e32 v[10:11], v[172:173]
	v_mov_b64_e32 v[12:13], v[174:175]
	v_mov_b32_e32 v31, v49
	v_pk_add_f32 v[40:41], v[48:49], v[30:31]
	v_pk_mov_b32 v[30:31], v[34:35], v[44:45] op_sel:[1,0]
	v_mov_b32_e32 v27, v44
	v_mov_b32_e32 v3, v7
	v_pk_add_f32 v[30:31], v[6:7], v[30:31]
	v_mov_b32_e32 v39, v33
	v_pk_add_f32 v[26:27], v[2:3], v[26:27]
	v_pk_add_f32 v[30:31], v[30:31], v[32:33]
	v_pk_add_f32 v[26:27], v[26:27], v[38:39]
	v_pk_mul_f32 v[32:33], v[46:47], v[46:47]
	v_pk_add_f32 v[34:35], v[30:31], v[26:27]
	v_pk_mul_f32 v[26:27], v[30:31], v[26:27]
	v_mov_b32_e32 v51, v33
	v_pk_mul_f32 v[32:33], v[48:49], v[48:49]
	v_mov_b32_e32 v35, v27
	v_pk_mul_f32 v[26:27], v[40:41], v[40:41]
	v_mov_b32_e32 v32, v40
	v_mov_b32_e32 v67, v26
	v_pk_add_f32 v[32:33], v[50:51], v[32:33]
	v_pk_add_f32 v[26:27], v[34:35], v[66:67]
	v_pk_mul_f32 v[30:31], v[36:37], v[36:37]
	v_pk_mul_f32 v[34:35], v[28:29], v[28:29]
	v_and_b32_e32 v23, 64, v108
	v_pk_add_f32 v[26:27], v[32:33], v[26:27]
	v_mov_b32_e32 v32, v36
	v_mov_b32_e32 v33, v30
	v_mov_b32_e32 v38, v28
	v_mov_b32_e32 v39, v34
	v_add_u32_e32 v23, 64, v23
	v_pk_add_f32 v[32:33], v[32:33], v[38:39]
	v_mov_b32_e32 v30, v37
	v_mov_b32_e32 v34, v29
	v_cmp_lt_i32_e64 s[0:1], v24, v23
	v_pk_add_f32 v[26:27], v[26:27], v[32:33]
	v_pk_add_f32 v[30:31], v[30:31], v[34:35]
	v_cndmask_b32_e64 v24, v108, v24, s[0:1]
	v_pk_add_f32 v[26:27], v[26:27], v[30:31]
	v_lshlrev_b32_e32 v30, 2, v24
	ds_bpermute_b32 v32, v30, v26
	ds_bpermute_b32 v33, v30, v27
	v_xor_b32_e32 v24, 4, v108
	v_cmp_lt_i32_e64 s[0:1], v24, v23
	v_cvt_pk_f16_f32 v39, v28, v29
	v_cvt_pk_f16_f32 v37, v36, v37
	v_cndmask_b32_e64 v24, v108, v24, s[0:1]
	s_waitcnt lgkmcnt(0)
	v_pk_add_f32 v[26:27], v[26:27], v[32:33]
	v_lshlrev_b32_e32 v31, 2, v24
	ds_bpermute_b32 v32, v31, v26
	ds_bpermute_b32 v33, v31, v27
	v_xor_b32_e32 v24, 2, v108
	v_cmp_lt_i32_e64 s[0:1], v24, v23
	v_cvt_pk_f16_f32 v36, v47, v50
	v_cvt_pk_f16_f32 v38, v49, v40
	v_cndmask_b32_e64 v24, v108, v24, s[0:1]
	s_waitcnt lgkmcnt(0)
	v_pk_add_f32 v[26:27], v[26:27], v[32:33]
	v_lshlrev_b32_e32 v33, 2, v24
	ds_bpermute_b32 v28, v33, v26
	ds_bpermute_b32 v29, v33, v27
	v_or_b32_e32 v32, s2, v78
	v_mul_lo_u32 v24, v25, s30
	v_add_lshl_u32 v24, v32, v24, 1
	buffer_store_dwordx4 v[36:39], v24, s[8:11], 0 offen sc1
	s_waitcnt lgkmcnt(0)
	v_pk_add_f32 v[26:27], v[26:27], v[28:29]
	v_xor_b32_e32 v28, 1, v108
	v_cmp_lt_i32_e64 s[0:1], v28, v23
	s_lshl_b32 s2, s15, 4
	v_mov_b32_e32 v24, v7
	v_cndmask_b32_e64 v23, v108, v28, s[0:1]
	v_lshlrev_b32_e32 v34, 2, v23
	ds_bpermute_b32 v28, v34, v26
	ds_bpermute_b32 v29, v34, v27
	s_and_saveexec_b64 s[0:1], vcc
	s_cbranch_execz .LBB9_5
	s_waitcnt lgkmcnt(0)
	v_pk_add_f32 v[64:65], v[26:27], v[28:29]
	v_lshl_add_u32 v23, v25, 6, s2
	v_mov_b32_e32 v67, v66
	s_mov_b32 s18, s10
	s_mov_b32 s19, s11
	buffer_store_dwordx4 v[64:67], v23, s[16:19], 0 offen sc1
.LBB9_5:
	s_or_b64 exec, exec, s[0:1]
	v_add_u32_e32 v23, 0, v88
	v_add_u32_e32 v25, s28, v88
	s_waitcnt lgkmcnt(0)
	ds_read_b128 v[26:29], v23
	ds_read_b128 v[36:39], v25
	v_add_u32_e32 v23, 0, v89
	v_add_u32_e32 v25, s28, v89
	ds_read_b128 v[40:43], v23
	ds_read_b128 v[44:47], v25
	v_cvt_f32_f16_e32 v50, v18
	s_waitcnt lgkmcnt(2)
	v_add_f32_e32 v49, v26, v36
	v_cvt_f32_f16_sdwa v51, v18 dst_sel:DWORD dst_unused:UNUSED_PAD src0_sel:WORD_1
	v_cvt_f32_f16_sdwa v55, v19 dst_sel:DWORD dst_unused:UNUSED_PAD src0_sel:WORD_1
	v_cvt_f32_f16_e32 v54, v19
	v_pk_mov_b32 v[26:27], v[26:27], v[6:7] op_sel:[1,0]
	v_mov_b32_e32 v48, v37
	v_cvt_f32_f16_e32 v52, v20
	v_pk_add_f32 v[26:27], v[26:27], v[48:49]
	v_pk_add_f32 v[28:29], v[28:29], v[38:39]
	v_pk_mov_b32 v[36:37], v[48:49], v[26:27] op_sel:[1,0]
	s_waitcnt lgkmcnt(0)
	v_add_f32_e32 v18, v40, v44
	v_pk_add_f32 v[28:29], v[8:9], v[28:29]
	v_pk_add_f32 v[36:37], v[6:7], v[36:37]
	v_mov_b32_e32 v25, v50
	v_cvt_f32_f16_sdwa v20, v20 dst_sel:DWORD dst_unused:UNUSED_PAD src0_sel:WORD_1
	v_pk_add_f32 v[28:29], v[28:29], v[54:55]
	v_mov_b32_e32 v19, v26
	v_pk_add_f32 v[54:55], v[24:25], v[26:27]
	v_pk_add_f32 v[26:27], v[36:37], v[50:51]
	v_pk_mov_b32 v[36:37], v[40:41], v[2:3] op_sel:[1,0]
	v_mov_b32_e32 v40, v45
	v_mov_b32_e32 v41, v18
	v_pk_add_f32 v[48:49], v[2:3], v[18:19]
	v_pk_add_f32 v[18:19], v[36:37], v[40:41]
	v_mov_b32_e32 v23, v52
	v_mov_b32_e32 v53, v51
	v_cvt_f32_f16_sdwa v57, v21 dst_sel:DWORD dst_unused:UNUSED_PAD src0_sel:WORD_1
	v_cvt_f32_f16_e32 v56, v21
	v_pk_add_f32 v[40:41], v[22:23], v[18:19]
	v_pk_add_f32 v[36:37], v[48:49], v[52:53]
	v_mov_b32_e32 v18, v51
	v_mov_b32_e32 v19, v55
	v_mov_b32_e32 v21, v41
	v_pk_add_f32 v[42:43], v[42:43], v[46:47]
	v_pk_add_f32 v[44:45], v[54:55], v[18:19]
	v_pk_mul_f32 v[18:19], v[54:55], v[54:55]
	v_pk_add_f32 v[48:49], v[40:41], v[20:21]
	v_pk_add_f32 v[20:21], v[26:27], v[36:37]
	v_pk_mul_f32 v[26:27], v[26:27], v[36:37]
	v_pk_add_f32 v[42:43], v[4:5], v[42:43]
	v_mov_b32_e32 v45, v19
	v_pk_mul_f32 v[18:19], v[40:41], v[40:41]
	v_mov_b32_e32 v21, v27
	v_pk_mul_f32 v[26:27], v[48:49], v[48:49]
	v_pk_add_f32 v[42:43], v[42:43], v[56:57]
	v_mov_b32_e32 v18, v48
	v_mov_b32_e32 v67, v26
	v_pk_mul_f32 v[38:39], v[28:29], v[28:29]
	v_pk_mul_f32 v[46:47], v[42:43], v[42:43]
	v_pk_add_f32 v[18:19], v[44:45], v[18:19]
	v_pk_add_f32 v[20:21], v[20:21], v[66:67]
	v_mov_b32_e32 v26, v42
	v_pk_add_f32 v[18:19], v[18:19], v[20:21]
	v_mov_b32_e32 v20, v28
	v_mov_b32_e32 v21, v38
	v_mov_b32_e32 v27, v46
	v_pk_add_f32 v[20:21], v[20:21], v[26:27]
	v_mov_b32_e32 v38, v29
	v_mov_b32_e32 v46, v43
	v_pk_add_f32 v[18:19], v[18:19], v[20:21]
	v_pk_add_f32 v[20:21], v[38:39], v[46:47]
	v_or_b32_e32 v23, s14, v87
	v_pk_add_f32 v[18:19], v[18:19], v[20:21]
	ds_bpermute_b32 v20, v30, v18
	ds_bpermute_b32 v21, v30, v19
	v_mul_lo_u32 v25, v23, s30
	v_cvt_pk_f16_f32 v27, v28, v29
	v_cvt_pk_f16_f32 v29, v42, v43
	v_add_lshl_u32 v25, v32, v25, 1
	s_waitcnt lgkmcnt(0)
	v_pk_add_f32 v[18:19], v[18:19], v[20:21]
	ds_bpermute_b32 v20, v31, v18
	ds_bpermute_b32 v21, v31, v19
	v_cvt_pk_f16_f32 v26, v55, v44
	v_cvt_pk_f16_f32 v28, v41, v48
	buffer_store_dwordx4 v[26:29], v25, s[8:11], 0 offen sc1
	s_waitcnt lgkmcnt(0)
	v_pk_add_f32 v[18:19], v[18:19], v[20:21]
	ds_bpermute_b32 v20, v33, v18
	ds_bpermute_b32 v21, v33, v19
	s_waitcnt lgkmcnt(0)
	v_pk_add_f32 v[18:19], v[18:19], v[20:21]
	ds_bpermute_b32 v20, v34, v18
	ds_bpermute_b32 v21, v34, v19
	s_and_saveexec_b64 s[0:1], vcc
	s_cbranch_execz .LBB9_7
	s_waitcnt lgkmcnt(0)
	v_pk_add_f32 v[64:65], v[18:19], v[20:21]
	v_lshl_add_u32 v18, v23, 6, s2
	v_mov_b32_e32 v67, v66
	s_mov_b32 s18, s10
	s_mov_b32 s19, s11
	buffer_store_dwordx4 v[64:67], v18, s[16:19], 0 offen sc1
.LBB9_7:
	s_or_b64 exec, exec, s[0:1]
	v_add_u32_e32 v18, 0, v91
	v_add_u32_e32 v23, s28, v91
	s_waitcnt lgkmcnt(0)
	ds_read_b128 v[18:21], v18
	ds_read_b128 v[26:29], v23
	v_add_u32_e32 v23, 0, v92
	v_add_u32_e32 v25, s28, v92
	ds_read_b128 v[36:39], v23
	ds_read_b128 v[40:43], v25
	v_cvt_f32_f16_e32 v46, v14
	v_cvt_f32_f16_e32 v48, v16
	s_waitcnt lgkmcnt(2)
	v_add_f32_e32 v45, v18, v26
	v_cvt_f32_f16_sdwa v47, v14 dst_sel:DWORD dst_unused:UNUSED_PAD src0_sel:WORD_1
	v_pk_mov_b32 v[18:19], v[18:19], v[6:7] op_sel:[1,0]
	v_mov_b32_e32 v44, v27
	s_waitcnt lgkmcnt(0)
	v_add_f32_e32 v14, v36, v40
	v_pk_add_f32 v[18:19], v[18:19], v[44:45]
	v_cvt_f32_f16_sdwa v16, v16 dst_sel:DWORD dst_unused:UNUSED_PAD src0_sel:WORD_1
	v_cvt_f32_f16_sdwa v51, v15 dst_sel:DWORD dst_unused:UNUSED_PAD src0_sel:WORD_1
	v_cvt_f32_f16_e32 v50, v15
	v_mov_b32_e32 v15, v18
	v_pk_mov_b32 v[36:37], v[36:37], v[2:3] op_sel:[1,0]
	v_mov_b32_e32 v40, v41
	v_mov_b32_e32 v41, v14
	v_pk_mov_b32 v[26:27], v[44:45], v[18:19] op_sel:[1,0]
	v_pk_add_f32 v[44:45], v[2:3], v[14:15]
	v_mov_b32_e32 v25, v46
	v_pk_add_f32 v[14:15], v[36:37], v[40:41]
	v_mov_b32_e32 v23, v48
	v_mov_b32_e32 v49, v47
	v_cvt_f32_f16_sdwa v53, v17 dst_sel:DWORD dst_unused:UNUSED_PAD src0_sel:WORD_1
	v_cvt_f32_f16_e32 v52, v17
	v_pk_add_f32 v[26:27], v[6:7], v[26:27]
	v_pk_add_f32 v[18:19], v[24:25], v[18:19]
	v_pk_add_f32 v[40:41], v[22:23], v[14:15]
	v_pk_add_f32 v[26:27], v[26:27], v[46:47]
	v_pk_add_f32 v[36:37], v[44:45], v[48:49]
	v_mov_b32_e32 v14, v47
	v_mov_b32_e32 v15, v19
	v_mov_b32_e32 v17, v41
	v_pk_add_f32 v[20:21], v[20:21], v[28:29]
	v_pk_add_f32 v[38:39], v[38:39], v[42:43]
	v_pk_add_f32 v[44:45], v[18:19], v[14:15]
	v_pk_mul_f32 v[14:15], v[18:19], v[18:19]
	v_pk_add_f32 v[46:47], v[40:41], v[16:17]
	v_pk_add_f32 v[16:17], v[26:27], v[36:37]
	v_pk_mul_f32 v[26:27], v[26:27], v[36:37]
	v_pk_add_f32 v[20:21], v[8:9], v[20:21]
	v_pk_add_f32 v[38:39], v[4:5], v[38:39]
	v_mov_b32_e32 v45, v15
	v_pk_mul_f32 v[14:15], v[40:41], v[40:41]
	v_mov_b32_e32 v17, v27
	v_pk_mul_f32 v[26:27], v[46:47], v[46:47]
	v_pk_add_f32 v[20:21], v[20:21], v[50:51]
	v_pk_add_f32 v[38:39], v[38:39], v[52:53]
	v_mov_b32_e32 v14, v46
	v_mov_b32_e32 v67, v26
	v_pk_mul_f32 v[28:29], v[20:21], v[20:21]
	v_pk_mul_f32 v[42:43], v[38:39], v[38:39]
	v_pk_add_f32 v[14:15], v[44:45], v[14:15]
	v_pk_add_f32 v[16:17], v[16:17], v[66:67]
	v_mov_b32_e32 v26, v38
	v_pk_add_f32 v[14:15], v[14:15], v[16:17]
	v_mov_b32_e32 v16, v20
	v_mov_b32_e32 v17, v28
	v_mov_b32_e32 v27, v42
	v_pk_add_f32 v[16:17], v[16:17], v[26:27]
	v_mov_b32_e32 v28, v21
	v_mov_b32_e32 v42, v39
	v_pk_add_f32 v[14:15], v[14:15], v[16:17]
	v_pk_add_f32 v[16:17], v[28:29], v[42:43]
	v_or_b32_e32 v18, s14, v90
	v_pk_add_f32 v[14:15], v[14:15], v[16:17]
	ds_bpermute_b32 v16, v30, v14
	ds_bpermute_b32 v17, v30, v15
	v_cvt_pk_f16_f32 v27, v20, v21
	v_mul_lo_u32 v20, v18, s30
	v_cvt_pk_f16_f32 v29, v38, v39
	v_add_lshl_u32 v20, v32, v20, 1
	s_waitcnt lgkmcnt(0)
	v_pk_add_f32 v[14:15], v[14:15], v[16:17]
	ds_bpermute_b32 v16, v31, v14
	ds_bpermute_b32 v17, v31, v15
	v_cvt_pk_f16_f32 v26, v19, v44
	v_cvt_pk_f16_f32 v28, v41, v46
	buffer_store_dwordx4 v[26:29], v20, s[8:11], 0 offen sc1
	s_waitcnt lgkmcnt(0)
	v_pk_add_f32 v[14:15], v[14:15], v[16:17]
	ds_bpermute_b32 v16, v33, v14
	ds_bpermute_b32 v17, v33, v15
	s_waitcnt lgkmcnt(0)
	v_pk_add_f32 v[14:15], v[14:15], v[16:17]
	ds_bpermute_b32 v16, v34, v14
	ds_bpermute_b32 v17, v34, v15
	s_and_saveexec_b64 s[0:1], vcc
	s_cbranch_execz .LBB9_9
	s_waitcnt lgkmcnt(0)
	v_pk_add_f32 v[64:65], v[14:15], v[16:17]
	v_lshl_add_u32 v14, v18, 6, s2
	v_mov_b32_e32 v67, v66
	s_mov_b32 s18, s10
	s_mov_b32 s19, s11
	buffer_store_dwordx4 v[64:67], v14, s[16:19], 0 offen sc1
.LBB9_9:
	s_or_b64 exec, exec, s[0:1]
	v_add_u32_e32 v14, 0, v94
	v_add_u32_e32 v18, s28, v94
	s_waitcnt lgkmcnt(0)
	ds_read_b128 v[14:17], v14
	ds_read_b128 v[18:21], v18
	v_add_u32_e32 v23, 0, v95
	v_add_u32_e32 v25, s28, v95
	ds_read_b128 v[26:29], v23
	ds_read_b128 v[36:39], v25
	v_cvt_f32_f16_e32 v42, v10
	s_waitcnt lgkmcnt(2)
	v_add_f32_e32 v41, v14, v18
	v_cvt_f32_f16_sdwa v43, v10 dst_sel:DWORD dst_unused:UNUSED_PAD src0_sel:WORD_1
	v_cvt_f32_f16_e32 v44, v12
	v_pk_mov_b32 v[14:15], v[14:15], v[6:7] op_sel:[1,0]
	v_mov_b32_e32 v40, v19
	v_pk_add_f32 v[14:15], v[14:15], v[40:41]
	s_waitcnt lgkmcnt(0)
	v_add_f32_e32 v10, v26, v36
	v_cvt_f32_f16_sdwa v47, v11 dst_sel:DWORD dst_unused:UNUSED_PAD src0_sel:WORD_1
	v_cvt_f32_f16_e32 v46, v11
	v_pk_mov_b32 v[18:19], v[40:41], v[14:15] op_sel:[1,0]
	v_mov_b32_e32 v11, v14
	v_mov_b32_e32 v25, v42
	v_cvt_f32_f16_sdwa v12, v12 dst_sel:DWORD dst_unused:UNUSED_PAD src0_sel:WORD_1
	v_pk_add_f32 v[6:7], v[6:7], v[18:19]
	v_pk_add_f32 v[18:19], v[2:3], v[10:11]
	v_pk_add_f32 v[14:15], v[24:25], v[14:15]
	v_pk_mov_b32 v[2:3], v[26:27], v[2:3] op_sel:[1,0]
	v_mov_b32_e32 v24, v37
	v_mov_b32_e32 v25, v10
	v_mov_b32_e32 v45, v43
	v_pk_add_f32 v[2:3], v[2:3], v[24:25]
	v_mov_b32_e32 v23, v44
	v_cvt_f32_f16_sdwa v49, v13 dst_sel:DWORD dst_unused:UNUSED_PAD src0_sel:WORD_1
	v_cvt_f32_f16_e32 v48, v13
	v_pk_add_f32 v[10:11], v[18:19], v[44:45]
	v_pk_add_f32 v[18:19], v[22:23], v[2:3]
	v_pk_add_f32 v[6:7], v[6:7], v[42:43]
	v_mov_b32_e32 v2, v43
	v_mov_b32_e32 v3, v15
	v_mov_b32_e32 v13, v19
	v_pk_add_f32 v[16:17], v[16:17], v[20:21]
	v_pk_add_f32 v[20:21], v[28:29], v[38:39]
	v_pk_add_f32 v[22:23], v[14:15], v[2:3]
	v_pk_mul_f32 v[2:3], v[14:15], v[14:15]
	v_pk_add_f32 v[12:13], v[18:19], v[12:13]
	v_pk_add_f32 v[24:25], v[6:7], v[10:11]
	v_pk_mul_f32 v[6:7], v[6:7], v[10:11]
	v_pk_add_f32 v[8:9], v[8:9], v[16:17]
	v_pk_add_f32 v[4:5], v[4:5], v[20:21]
	v_mov_b32_e32 v23, v3
	v_pk_mul_f32 v[2:3], v[18:19], v[18:19]
	v_mov_b32_e32 v25, v7
	v_pk_mul_f32 v[6:7], v[12:13], v[12:13]
	v_pk_add_f32 v[8:9], v[8:9], v[46:47]
	v_pk_add_f32 v[4:5], v[4:5], v[48:49]
	v_mov_b32_e32 v2, v12
	v_mov_b32_e32 v67, v6
	v_pk_mul_f32 v[16:17], v[8:9], v[8:9]
	v_pk_mul_f32 v[20:21], v[4:5], v[4:5]
	v_pk_add_f32 v[2:3], v[22:23], v[2:3]
	v_pk_add_f32 v[6:7], v[24:25], v[66:67]
	v_mov_b32_e32 v10, v4
	v_pk_add_f32 v[2:3], v[2:3], v[6:7]
	v_mov_b32_e32 v6, v8
	v_mov_b32_e32 v7, v16
	v_mov_b32_e32 v11, v20
	v_pk_add_f32 v[6:7], v[6:7], v[10:11]
	v_mov_b32_e32 v16, v9
	v_mov_b32_e32 v20, v5
	v_pk_add_f32 v[2:3], v[2:3], v[6:7]
	v_pk_add_f32 v[6:7], v[16:17], v[20:21]
	v_cvt_pk_f16_f32 v11, v4, v5
	v_pk_add_f32 v[2:3], v[2:3], v[6:7]
	ds_bpermute_b32 v6, v30, v2
	ds_bpermute_b32 v7, v30, v3
	v_cvt_pk_f16_f32 v9, v8, v9
	v_cvt_pk_f16_f32 v8, v15, v22
	v_cvt_pk_f16_f32 v10, v19, v12
	s_waitcnt lgkmcnt(0)
	v_pk_add_f32 v[2:3], v[2:3], v[6:7]
	ds_bpermute_b32 v6, v31, v2
	ds_bpermute_b32 v7, v31, v3
	s_waitcnt lgkmcnt(0)
	v_pk_add_f32 v[2:3], v[2:3], v[6:7]
	ds_bpermute_b32 v16, v33, v2
	ds_bpermute_b32 v17, v33, v3
	v_add_u32_e32 v6, s14, v93
	v_mul_lo_u32 v7, v6, s30
	v_add_lshl_u32 v7, v32, v7, 1
	buffer_store_dwordx4 v[8:11], v7, s[8:11], 0 offen sc1
	s_waitcnt lgkmcnt(0)
	v_pk_add_f32 v[2:3], v[2:3], v[16:17]
	ds_bpermute_b32 v4, v34, v2
	ds_bpermute_b32 v5, v34, v3
	s_and_saveexec_b64 s[0:1], vcc
	s_cbranch_execz .LBB9_2
	s_waitcnt lgkmcnt(0)
	v_pk_add_f32 v[64:65], v[2:3], v[4:5]
	v_lshl_add_u32 v2, v6, 6, s2
	v_mov_b32_e32 v67, v66
	s_mov_b32 s18, s10
	s_mov_b32 s19, s11
	buffer_store_dwordx4 v[64:67], v2, s[16:19], 0 offen sc1
	s_branch .LBB9_2

	.amdhsa_kernel _Z6gemm_pILi2ELi32EEvPKDF16_S1_iiiiiiPKfS3_S3_PfPDF16_S4_S5_S4_
		.amdhsa_group_segment_fixed_size 0
		.amdhsa_private_segment_fixed_size 0
		.amdhsa_kernarg_size 360
		.amdhsa_user_sgpr_count 2
		.amdhsa_user_sgpr_dispatch_ptr 0
		.amdhsa_user_sgpr_queue_ptr 0
		.amdhsa_user_sgpr_kernarg_segment_ptr 1
		.amdhsa_user_sgpr_dispatch_id 0
		.amdhsa_user_sgpr_kernarg_preload_length 0
		.amdhsa_user_sgpr_kernarg_preload_offset 0
		.amdhsa_user_sgpr_private_segment_size 0
		.amdhsa_uses_dynamic_stack 0
		.amdhsa_enable_private_segment 0
		.amdhsa_system_sgpr_workgroup_id_x 1
		.amdhsa_system_sgpr_workgroup_id_y 0
		.amdhsa_system_sgpr_workgroup_id_z 0
		.amdhsa_system_sgpr_workgroup_info 0
		.amdhsa_system_vgpr_workitem_id 0
		.amdhsa_next_free_vgpr 192
		.amdhsa_next_free_sgpr 52
		.amdhsa_accum_offset 192
		.amdhsa_reserve_vcc 1
		.amdhsa_float_round_mode_32 0
		.amdhsa_float_round_mode_16_64 0
		.amdhsa_float_denorm_mode_32 3
		.amdhsa_float_denorm_mode_16_64 3
		.amdhsa_dx10_clamp 1
		.amdhsa_ieee_mode 1
		.amdhsa_fp16_overflow 0
		.amdhsa_tg_split 0
		.amdhsa_exception_fp_ieee_invalid_op 0
		.amdhsa_exception_fp_denorm_src 0
		.amdhsa_exception_fp_ieee_div_zero 0
		.amdhsa_exception_fp_ieee_overflow 0
		.amdhsa_exception_fp_ieee_underflow 0
		.amdhsa_exception_fp_ieee_inexact 0
		.amdhsa_exception_int_div_zero 0
	.end_amdhsa_kernel

amdhsa.kernels:
  - .agpr_count:     0
    .args:
      - .actual_access:  read_only
        .address_space:  global
        .offset:         0
        .size:           8
        .value_kind:     global_buffer
      - .actual_access:  read_only
        .address_space:  global
        .offset:         8
        .size:           8
        .value_kind:     global_buffer
      - .actual_access:  read_only
        .address_space:  global
        .offset:         16
        .size:           8
        .value_kind:     global_buffer
      - .actual_access:  read_only
        .address_space:  global
        .offset:         24
        .size:           8
        .value_kind:     global_buffer
      - .actual_access:  write_only
        .address_space:  global
        .offset:         32
        .size:           8
        .value_kind:     global_buffer
      - .actual_access:  write_only
        .address_space:  global
        .offset:         40
        .size:           8
        .value_kind:     global_buffer
    .group_segment_fixed_size: 0
    .kernarg_segment_align: 8
    .kernarg_segment_size: 48
    .language:       OpenCL C
    .language_version:
      - 2
      - 0
    .max_flat_workgroup_size: 256
    .name:           _Z9fold_sumsPKfS0_S0_S0_PfS1_
    .private_segment_fixed_size: 0
    .sgpr_count:     15
    .sgpr_spill_count: 0
    .symbol:         _Z9fold_sumsPKfS0_S0_S0_PfS1_.kd
    .uniform_work_group_size: 1
    .uses_dynamic_stack: false
    .vgpr_count:     24
    .vgpr_spill_count: 0
    .wavefront_size: 64
  - .agpr_count:     0
    .args:
      - .offset:         0
        .size:           208
        .value_kind:     by_value
    .group_segment_fixed_size: 10496
    .kernarg_segment_align: 8
    .kernarg_segment_size: 208
    .language:       OpenCL C
    .language_version:
      - 2
      - 0
    .max_flat_workgroup_size: 256
    .name:           _Z15prologue_kernel12PrologueArgs
    .private_segment_fixed_size: 0
    .sgpr_count:     30
    .sgpr_spill_count: 0
    .symbol:         _Z15prologue_kernel12PrologueArgs.kd
    .uniform_work_group_size: 1
    .uses_dynamic_stack: false
    .vgpr_count:     35
    .vgpr_spill_count: 0
    .wavefront_size: 64
  - .agpr_count:     0
    .args:
      - .address_space:  global
        .offset:         0
        .size:           8
        .value_kind:     global_buffer
      - .address_space:  global
        .offset:         8
        .size:           8
        .value_kind:     global_buffer
      - .actual_access:  read_only
        .address_space:  global
        .offset:         16
        .size:           8
        .value_kind:     global_buffer
      - .actual_access:  read_only
        .address_space:  global
        .offset:         24
        .size:           8
        .value_kind:     global_buffer
      - .actual_access:  read_only
        .address_space:  global
        .offset:         32
        .size:           8
        .value_kind:     global_buffer
      - .actual_access:  write_only
        .address_space:  global
        .offset:         40
        .size:           8
        .value_kind:     global_buffer
      - .actual_access:  write_only
        .address_space:  global
        .offset:         48
        .size:           8
        .value_kind:     global_buffer
      - .offset:         56
        .size:           4
        .value_kind:     by_value
      - .offset:         60
        .size:           4
        .value_kind:     by_value
    .group_segment_fixed_size: 0
    .kernarg_segment_align: 8
    .kernarg_segment_size: 64
    .language:       OpenCL C
    .language_version:
      - 2
      - 0
    .max_flat_workgroup_size: 512
    .name:           _Z11attn_kernelPKDF16_PDF16_PKfS3_S3_PfS4_ii
    .private_segment_fixed_size: 0
    .sgpr_count:     34
    .sgpr_spill_count: 0
    .symbol:         _Z11attn_kernelPKDF16_PDF16_PKfS3_S3_PfS4_ii.kd
    .uniform_work_group_size: 1
    .uses_dynamic_stack: false
    .vgpr_count:     128
    .vgpr_spill_count: 0
    .wavefront_size: 64
  - .agpr_count:     0
    .args:
      - .actual_access:  read_only
        .address_space:  global
        .offset:         0
        .size:           8
        .value_kind:     global_buffer
      - .actual_access:  read_only
        .address_space:  global
        .offset:         8
        .size:           8
        .value_kind:     global_buffer
      - .actual_access:  write_only
        .address_space:  global
        .offset:         16
        .size:           8
        .value_kind:     global_buffer
    .group_segment_fixed_size: 64
    .kernarg_segment_align: 8
    .kernarg_segment_size: 24
    .language:       OpenCL C
    .language_version:
      - 2
      - 0
    .max_flat_workgroup_size: 1024
    .name:           _Z12loss_combinePKfS0_Pf
    .private_segment_fixed_size: 0
    .sgpr_count:     20
    .sgpr_spill_count: 0
    .symbol:         _Z12loss_combinePKfS0_Pf.kd
    .uniform_work_group_size: 1
    .uses_dynamic_stack: false
    .vgpr_count:     17
    .vgpr_spill_count: 0
    .wavefront_size: 64
  - .agpr_count:     0
    .args:
      - .actual_access:  read_only
        .address_space:  global
        .offset:         0
        .size:           8
        .value_kind:     global_buffer
      - .actual_access:  read_only
        .address_space:  global
        .offset:         8
        .size:           8
        .value_kind:     global_buffer
      - .actual_access:  write_only
        .address_space:  global
        .offset:         16
        .size:           8
        .value_kind:     global_buffer
    .group_segment_fixed_size: 16
    .kernarg_segment_align: 8
    .kernarg_segment_size: 24
    .language:       OpenCL C
    .language_version:
      - 2
      - 0
    .max_flat_workgroup_size: 256
    .name:           _Z9loss_rowsPKfPKiPf
    .private_segment_fixed_size: 0
    .sgpr_count:     18
    .sgpr_spill_count: 0
    .symbol:         _Z9loss_rowsPKfPKiPf.kd
    .uniform_work_group_size: 1
    .uses_dynamic_stack: false
    .vgpr_count:     28
    .vgpr_spill_count: 0
    .wavefront_size: 64
  - .agpr_count:     0
    .args:
      - .actual_access:  read_only
        .address_space:  global
        .offset:         0
        .size:           8
        .value_kind:     global_buffer
      - .actual_access:  write_only
        .address_space:  global
        .offset:         8
        .size:           8
        .value_kind:     global_buffer
    .group_segment_fixed_size: 16
    .kernarg_segment_align: 8
    .kernarg_segment_size: 16
    .language:       OpenCL C
    .language_version:
      - 2
      - 0
    .max_flat_workgroup_size: 256
    .name:           _Z10loss_finalPKfPf
    .private_segment_fixed_size: 0
    .sgpr_count:     10
    .sgpr_spill_count: 0
    .symbol:         _Z10loss_finalPKfPf.kd
    .uniform_work_group_size: 1
    .uses_dynamic_stack: false
    .vgpr_count:     6
    .vgpr_spill_count: 0
    .wavefront_size: 64
  - .agpr_count:     0
    .args:
      - .address_space:  global
        .offset:         0
        .size:           8
        .value_kind:     global_buffer
      - .address_space:  global
        .offset:         8
        .size:           8
        .value_kind:     global_buffer
      - .offset:         16
        .size:           4
        .value_kind:     by_value
      - .offset:         20
        .size:           4
        .value_kind:     by_value
      - .offset:         24
        .size:           4
        .value_kind:     by_value
      - .offset:         28
        .size:           4
        .value_kind:     by_value
      - .offset:         32
        .size:           4
        .value_kind:     by_value
      - .offset:         36
        .size:           4
        .value_kind:     by_value
      - .actual_access:  read_only
        .address_space:  global
        .offset:         40
        .size:           8
        .value_kind:     global_buffer
      - .actual_access:  read_only
        .address_space:  global
        .offset:         48
        .size:           8
        .value_kind:     global_buffer
      - .actual_access:  read_only
        .address_space:  global
        .offset:         56
        .size:           8
        .value_kind:     global_buffer
      - .actual_access:  read_only
        .address_space:  global
        .offset:         64
        .size:           8
        .value_kind:     global_buffer
      - .actual_access:  write_only
        .address_space:  global
        .offset:         72
        .size:           8
        .value_kind:     global_buffer
      - .offset:         80
        .size:           144
        .value_kind:     by_value
    .group_segment_fixed_size: 0
    .kernarg_segment_align: 8
    .kernarg_segment_size: 224
    .language:       OpenCL C
    .language_version:
      - 2
      - 0
    .max_flat_workgroup_size: 512
    .name:           _Z6gemm_qILi0ELi1EEvPKDF16_S1_iiiiiiPKfS3_S3_S3_PDF16_8ConvArgs
    .private_segment_fixed_size: 0
    .sgpr_count:     50
    .sgpr_spill_count: 0
    .symbol:         _Z6gemm_qILi0ELi1EEvPKDF16_S1_iiiiiiPKfS3_S3_S3_PDF16_8ConvArgs.kd
    .uniform_work_group_size: 1
    .uses_dynamic_stack: false
    .vgpr_count:     244
    .vgpr_spill_count: 0
    .wavefront_size: 64
  - .agpr_count:     0
    .args:
      - .actual_access:  read_only
        .address_space:  global
        .offset:         0
        .size:           8
        .value_kind:     global_buffer
      - .actual_access:  read_only
        .address_space:  global
        .offset:         8
        .size:           8
        .value_kind:     global_buffer
      - .offset:         16
        .size:           4
        .value_kind:     by_value
      - .offset:         20
        .size:           4
        .value_kind:     by_value
      - .offset:         24
        .size:           4
        .value_kind:     by_value
      - .offset:         28
        .size:           4
        .value_kind:     by_value
      - .offset:         32
        .size:           4
        .value_kind:     by_value
      - .offset:         36
        .size:           4
        .value_kind:     by_value
      - .actual_access:  read_only
        .address_space:  global
        .offset:         40
        .size:           8
        .value_kind:     global_buffer
      - .actual_access:  read_only
        .address_space:  global
        .offset:         48
        .size:           8
        .value_kind:     global_buffer
      - .actual_access:  read_only
        .address_space:  global
        .offset:         56
        .size:           8
        .value_kind:     global_buffer
      - .address_space:  global
        .offset:         64
        .size:           8
        .value_kind:     global_buffer
      - .address_space:  global
        .offset:         72
        .size:           8
        .value_kind:     global_buffer
      - .actual_access:  write_only
        .address_space:  global
        .offset:         80
        .size:           8
        .value_kind:     global_buffer
      - .actual_access:  read_only
        .address_space:  global
        .offset:         88
        .size:           8
        .value_kind:     global_buffer
      - .actual_access:  read_only
        .address_space:  global
        .offset:         96
        .size:           8
        .value_kind:     global_buffer
      - .offset:         104
        .size:           4
        .value_kind:     hidden_block_count_x
      - .offset:         108
        .size:           4
        .value_kind:     hidden_block_count_y
      - .offset:         112
        .size:           4
        .value_kind:     hidden_block_count_z
      - .offset:         116
        .size:           2
        .value_kind:     hidden_group_size_x
      - .offset:         118
        .size:           2
        .value_kind:     hidden_group_size_y
      - .offset:         120
        .size:           2
        .value_kind:     hidden_group_size_z
      - .offset:         122
        .size:           2
        .value_kind:     hidden_remainder_x
      - .offset:         124
        .size:           2
        .value_kind:     hidden_remainder_y
      - .offset:         126
        .size:           2
        .value_kind:     hidden_remainder_z
      - .offset:         144
        .size:           8
        .value_kind:     hidden_global_offset_x
      - .offset:         152
        .size:           8
        .value_kind:     hidden_global_offset_y
      - .offset:         160
        .size:           8
        .value_kind:     hidden_global_offset_z
      - .offset:         168
        .size:           2
        .value_kind:     hidden_grid_dims
      - .offset:         224
        .size:           4
        .value_kind:     hidden_dynamic_lds_size
    .group_segment_fixed_size: 0
    .kernarg_segment_align: 8
    .kernarg_segment_size: 360
    .language:       OpenCL C
    .language_version:
      - 2
      - 0
    .max_flat_workgroup_size: 512
    .name:           _Z6gemm_pILi2ELi8EEvPKDF16_S1_iiiiiiPKfS3_S3_PfPDF16_S4_S5_S4_
    .private_segment_fixed_size: 0
    .sgpr_count:     58
    .sgpr_spill_count: 0
    .symbol:         _Z6gemm_pILi2ELi8EEvPKDF16_S1_iiiiiiPKfS3_S3_PfPDF16_S4_S5_S4_.kd
    .uniform_work_group_size: 1
    .uses_dynamic_stack: false
    .vgpr_count:     192
    .vgpr_spill_count: 0
    .wavefront_size: 64
  - .agpr_count:     0
    .args:
      - .address_space:  global
        .offset:         0
        .size:           8
        .value_kind:     global_buffer
      - .address_space:  global
        .offset:         8
        .size:           8
        .value_kind:     global_buffer
      - .offset:         16
        .size:           4
        .value_kind:     by_value
      - .offset:         20
        .size:           4
        .value_kind:     by_value
      - .offset:         24
        .size:           4
        .value_kind:     by_value
      - .offset:         28
        .size:           4
        .value_kind:     by_value
      - .offset:         32
        .size:           4
        .value_kind:     by_value
      - .offset:         36
        .size:           4
        .value_kind:     by_value
      - .actual_access:  read_only
        .address_space:  global
        .offset:         40
        .size:           8
        .value_kind:     global_buffer
      - .actual_access:  read_only
        .address_space:  global
        .offset:         48
        .size:           8
        .value_kind:     global_buffer
      - .actual_access:  read_only
        .address_space:  global
        .offset:         56
        .size:           8
        .value_kind:     global_buffer
      - .actual_access:  read_only
        .address_space:  global
        .offset:         64
        .size:           8
        .value_kind:     global_buffer
      - .actual_access:  write_only
        .address_space:  global
        .offset:         72
        .size:           8
        .value_kind:     global_buffer
      - .offset:         80
        .size:           144
        .value_kind:     by_value
    .group_segment_fixed_size: 0
    .kernarg_segment_align: 8
    .kernarg_segment_size: 224
    .language:       OpenCL C
    .language_version:
      - 2
      - 0
    .max_flat_workgroup_size: 512
    .name:           _Z6gemm_qILi1ELi0EEvPKDF16_S1_iiiiiiPKfS3_S3_S3_PDF16_8ConvArgs
    .private_segment_fixed_size: 0
    .sgpr_count:     29
    .sgpr_spill_count: 0
    .symbol:         _Z6gemm_qILi1ELi0EEvPKDF16_S1_iiiiiiPKfS3_S3_S3_PDF16_8ConvArgs.kd
    .uniform_work_group_size: 1
    .uses_dynamic_stack: false
    .vgpr_count:     244
    .vgpr_spill_count: 0
    .wavefront_size: 64
  - .agpr_count:     0
    .args:
      - .actual_access:  read_only
        .address_space:  global
        .offset:         0
        .size:           8
        .value_kind:     global_buffer
      - .actual_access:  read_only
        .address_space:  global
        .offset:         8
        .size:           8
        .value_kind:     global_buffer
      - .offset:         16
        .size:           4
        .value_kind:     by_value
      - .offset:         20
        .size:           4
        .value_kind:     by_value
      - .offset:         24
        .size:           4
        .value_kind:     by_value
      - .offset:         28
        .size:           4
        .value_kind:     by_value
      - .offset:         32
        .size:           4
        .value_kind:     by_value
      - .offset:         36
        .size:           4
        .value_kind:     by_value
      - .actual_access:  read_only
        .address_space:  global
        .offset:         40
        .size:           8
        .value_kind:     global_buffer
      - .actual_access:  read_only
        .address_space:  global
        .offset:         48
        .size:           8
        .value_kind:     global_buffer
      - .actual_access:  read_only
        .address_space:  global
        .offset:         56
        .size:           8
        .value_kind:     global_buffer
      - .address_space:  global
        .offset:         64
        .size:           8
        .value_kind:     global_buffer
      - .address_space:  global
        .offset:         72
        .size:           8
        .value_kind:     global_buffer
      - .actual_access:  write_only
        .address_space:  global
        .offset:         80
        .size:           8
        .value_kind:     global_buffer
      - .actual_access:  read_only
        .address_space:  global
        .offset:         88
        .size:           8
        .value_kind:     global_buffer
      - .actual_access:  read_only
        .address_space:  global
        .offset:         96
        .size:           8
        .value_kind:     global_buffer
      - .offset:         104
        .size:           4
        .value_kind:     hidden_block_count_x
      - .offset:         108
        .size:           4
        .value_kind:     hidden_block_count_y
      - .offset:         112
        .size:           4
        .value_kind:     hidden_block_count_z
      - .offset:         116
        .size:           2
        .value_kind:     hidden_group_size_x
      - .offset:         118
        .size:           2
        .value_kind:     hidden_group_size_y
      - .offset:         120
        .size:           2
        .value_kind:     hidden_group_size_z
      - .offset:         122
        .size:           2
        .value_kind:     hidden_remainder_x
      - .offset:         124
        .size:           2
        .value_kind:     hidden_remainder_y
      - .offset:         126
        .size:           2
        .value_kind:     hidden_remainder_z
      - .offset:         144
        .size:           8
        .value_kind:     hidden_global_offset_x
      - .offset:         152
        .size:           8
        .value_kind:     hidden_global_offset_y
      - .offset:         160
        .size:           8
        .value_kind:     hidden_global_offset_z
      - .offset:         168
        .size:           2
        .value_kind:     hidden_grid_dims
      - .offset:         224
        .size:           4
        .value_kind:     hidden_dynamic_lds_size
    .group_segment_fixed_size: 0
    .kernarg_segment_align: 8
    .kernarg_segment_size: 360
    .language:       OpenCL C
    .language_version:
      - 2
      - 0
    .max_flat_workgroup_size: 512
    .name:           _Z6gemm_pILi2ELi32EEvPKDF16_S1_iiiiiiPKfS3_S3_PfPDF16_S4_S5_S4_
    .private_segment_fixed_size: 0
    .sgpr_count:     58
    .sgpr_spill_count: 0
    .symbol:         _Z6gemm_pILi2ELi32EEvPKDF16_S1_iiiiiiPKfS3_S3_PfPDF16_S4_S5_S4_.kd
    .uniform_work_group_size: 1
    .uses_dynamic_stack: false
    .vgpr_count:     192
    .vgpr_spill_count: 0
    .wavefront_size: 64
  - .agpr_count:     0
    .args:
      - .actual_access:  read_only
        .address_space:  global
        .offset:         0
        .size:           8
        .value_kind:     global_buffer
      - .actual_access:  read_only
        .address_space:  global
        .offset:         8
        .size:           8
        .value_kind:     global_buffer
      - .offset:         16
        .size:           4
        .value_kind:     by_value
      - .offset:         20
        .size:           4
        .value_kind:     by_value
      - .offset:         24
        .size:           4
        .value_kind:     by_value
      - .offset:         28
        .size:           4
        .value_kind:     by_value
      - .offset:         32
        .size:           4
        .value_kind:     by_value
      - .offset:         36
        .size:           4
        .value_kind:     by_value
      - .actual_access:  read_only
        .address_space:  global
        .offset:         40
        .size:           8
        .value_kind:     global_buffer
      - .actual_access:  read_only
        .address_space:  global
        .offset:         48
        .size:           8
        .value_kind:     global_buffer
      - .actual_access:  read_only
        .address_space:  global
        .offset:         56
        .size:           8
        .value_kind:     global_buffer
      - .address_space:  global
        .offset:         64
        .size:           8
        .value_kind:     global_buffer
      - .actual_access:  read_only
        .address_space:  global
        .offset:         72
        .size:           8
        .value_kind:     global_buffer
      - .actual_access:  write_only
        .address_space:  global
        .offset:         80
        .size:           8
        .value_kind:     global_buffer
      - .actual_access:  read_only
        .address_space:  global
        .offset:         88
        .size:           8
        .value_kind:     global_buffer
      - .actual_access:  write_only
        .address_space:  global
        .offset:         96
        .size:           8
        .value_kind:     global_buffer
      - .offset:         104
        .size:           4
        .value_kind:     hidden_block_count_x
      - .offset:         108
        .size:           4
        .value_kind:     hidden_block_count_y
      - .offset:         112
        .size:           4
        .value_kind:     hidden_block_count_z
      - .offset:         116
        .size:           2
        .value_kind:     hidden_group_size_x
      - .offset:         118
        .size:           2
        .value_kind:     hidden_group_size_y
      - .offset:         120
        .size:           2
        .value_kind:     hidden_group_size_z
      - .offset:         122
        .size:           2
        .value_kind:     hidden_remainder_x
      - .offset:         124
        .size:           2
        .value_kind:     hidden_remainder_y
      - .offset:         126
        .size:           2
        .value_kind:     hidden_remainder_z
      - .offset:         144
        .size:           8
        .value_kind:     hidden_global_offset_x
      - .offset:         152
        .size:           8
        .value_kind:     hidden_global_offset_y
      - .offset:         160
        .size:           8
        .value_kind:     hidden_global_offset_z
      - .offset:         168
        .size:           2
        .value_kind:     hidden_grid_dims
      - .offset:         224
        .size:           4
        .value_kind:     hidden_dynamic_lds_size
    .group_segment_fixed_size: 0
    .kernarg_segment_align: 8
    .kernarg_segment_size: 360
    .language:       OpenCL C
    .language_version:
      - 2
      - 0
    .max_flat_workgroup_size: 512
    .name:           _Z6gemm_pILi3ELi8EEvPKDF16_S1_iiiiiiPKfS3_S3_PfPDF16_S4_S5_S4_
    .private_segment_fixed_size: 0
    .sgpr_count:     46
    .sgpr_spill_count: 0
    .symbol:         _Z6gemm_pILi3ELi8EEvPKDF16_S1_iiiiiiPKfS3_S3_PfPDF16_S4_S5_S4_.kd
    .uniform_work_group_size: 1
    .uses_dynamic_stack: false
    .vgpr_count:     148
    .vgpr_spill_count: 0
    .wavefront_size: 64
